# i8 weight conversion: row-group-major order with progressive vmcnt(12/8/4/0) waits so conversion overlaps the tile loads' arrival (all 10 pool sites), on top of v058
# speedup vs baseline: 1.0038x; 1.0038x over previous
.LBB0_60:
	s_mov_b32 s17, s35
	s_mov_b32 s24, s70
	s_mov_b32 s16, s34
	s_mov_b32 s22, s26
	s_mov_b32 s23, s27
	s_mov_b32 s21, s25
	s_mov_b64 s[18:19], s[68:69]
	s_mov_b64 s[30:31], -1
	s_mov_b64 s[2:3], 0
	s_cmp_lt_i32 s35, 2
	s_mov_b64 s[28:29], 0
	s_cbranch_scc1 .LBB0_67
	s_cmp_eq_u32 s17, 2
	s_mov_b64 s[28:29], -1
	s_cbranch_scc0 .LBB0_63
	s_waitcnt vmcnt(12)
	v_mov_b32_e32 v88, 0x4b400000
	v_mov_b32_e32 v89, 0x4b40007f
	v_mov_b32_e32 v90, 0x4b3fff81
	v_mov_b32_e32 v91, 0xc0c0400
	v_add_u32_e32 v72, v78, v77
	v_fmamk_f32 v2, v2, 0x44800000, v88
	v_fmamk_f32 v6, v6, 0x44800000, v88
	v_fmamk_f32 v10, v10, 0x44800000, v88
	v_fmamk_f32 v14, v14, 0x44800000, v88
	v_med3_f32 v2, v2, v90, v89
	v_med3_f32 v6, v6, v90, v89
	v_med3_f32 v10, v10, v90, v89
	v_med3_f32 v14, v14, v90, v89
	v_perm_b32 v2, v6, v2, v91
	v_perm_b32 v10, v14, v10, v91
	v_lshl_or_b32 v66, v10, 16, v2
	v_fmamk_f32 v3, v3, 0x44800000, v88
	v_fmamk_f32 v7, v7, 0x44800000, v88
	v_fmamk_f32 v11, v11, 0x44800000, v88
	v_fmamk_f32 v15, v15, 0x44800000, v88
	v_med3_f32 v3, v3, v90, v89
	v_med3_f32 v7, v7, v90, v89
	v_med3_f32 v11, v11, v90, v89
	v_med3_f32 v15, v15, v90, v89
	v_perm_b32 v3, v7, v3, v91
	v_perm_b32 v11, v15, v11, v91
	v_lshl_or_b32 v218, v11, 16, v3
	v_fmamk_f32 v4, v4, 0x44800000, v88
	v_fmamk_f32 v8, v8, 0x44800000, v88
	v_fmamk_f32 v12, v12, 0x44800000, v88
	v_fmamk_f32 v16, v16, 0x44800000, v88
	v_med3_f32 v4, v4, v90, v89
	v_med3_f32 v8, v8, v90, v89
	v_med3_f32 v12, v12, v90, v89
	v_med3_f32 v16, v16, v90, v89
	v_perm_b32 v4, v8, v4, v91
	v_perm_b32 v12, v16, v12, v91
	v_lshl_or_b32 v222, v12, 16, v4
	v_fmamk_f32 v5, v5, 0x44800000, v88
	v_fmamk_f32 v9, v9, 0x44800000, v88
	v_fmamk_f32 v13, v13, 0x44800000, v88
	v_fmamk_f32 v17, v17, 0x44800000, v88
	v_med3_f32 v5, v5, v90, v89
	v_med3_f32 v9, v9, v90, v89
	v_med3_f32 v13, v13, v90, v89
	v_med3_f32 v17, v17, v90, v89
	v_perm_b32 v5, v9, v5, v91
	v_perm_b32 v13, v17, v13, v91
	v_lshl_or_b32 v226, v13, 16, v5
	s_waitcnt vmcnt(8)
	v_fmamk_f32 v18, v18, 0x44800000, v88
	v_fmamk_f32 v22, v22, 0x44800000, v88
	v_fmamk_f32 v26, v26, 0x44800000, v88
	v_fmamk_f32 v30, v30, 0x44800000, v88
	v_med3_f32 v18, v18, v90, v89
	v_med3_f32 v22, v22, v90, v89
	v_med3_f32 v26, v26, v90, v89
	v_med3_f32 v30, v30, v90, v89
	v_perm_b32 v18, v22, v18, v91
	v_perm_b32 v26, v30, v26, v91
	v_lshl_or_b32 v67, v26, 16, v18
	v_fmamk_f32 v19, v19, 0x44800000, v88
	v_fmamk_f32 v23, v23, 0x44800000, v88
	v_fmamk_f32 v27, v27, 0x44800000, v88
	v_fmamk_f32 v31, v31, 0x44800000, v88
	v_med3_f32 v19, v19, v90, v89
	v_med3_f32 v23, v23, v90, v89
	v_med3_f32 v27, v27, v90, v89
	v_med3_f32 v31, v31, v90, v89
	v_perm_b32 v19, v23, v19, v91
	v_perm_b32 v27, v31, v27, v91
	v_lshl_or_b32 v219, v27, 16, v19
	v_fmamk_f32 v20, v20, 0x44800000, v88
	v_fmamk_f32 v24, v24, 0x44800000, v88
	v_fmamk_f32 v28, v28, 0x44800000, v88
	v_fmamk_f32 v32, v32, 0x44800000, v88
	v_med3_f32 v20, v20, v90, v89
	v_med3_f32 v24, v24, v90, v89
	v_med3_f32 v28, v28, v90, v89
	v_med3_f32 v32, v32, v90, v89
	v_perm_b32 v20, v24, v20, v91
	v_perm_b32 v28, v32, v28, v91
	v_lshl_or_b32 v223, v28, 16, v20
	v_fmamk_f32 v21, v21, 0x44800000, v88
	v_fmamk_f32 v25, v25, 0x44800000, v88
	v_fmamk_f32 v29, v29, 0x44800000, v88
	v_fmamk_f32 v33, v33, 0x44800000, v88
	v_med3_f32 v21, v21, v90, v89
	v_med3_f32 v25, v25, v90, v89
	v_med3_f32 v29, v29, v90, v89
	v_med3_f32 v33, v33, v90, v89
	v_perm_b32 v21, v25, v21, v91
	v_perm_b32 v29, v33, v29, v91
	v_lshl_or_b32 v227, v29, 16, v21
	s_waitcnt vmcnt(4)
	v_fmamk_f32 v34, v34, 0x44800000, v88
	v_fmamk_f32 v38, v38, 0x44800000, v88
	v_fmamk_f32 v42, v42, 0x44800000, v88
	v_fmamk_f32 v46, v46, 0x44800000, v88
	v_med3_f32 v34, v34, v90, v89
	v_med3_f32 v38, v38, v90, v89
	v_med3_f32 v42, v42, v90, v89
	v_med3_f32 v46, v46, v90, v89
	v_perm_b32 v34, v38, v34, v91
	v_perm_b32 v42, v46, v42, v91
	v_lshl_or_b32 v68, v42, 16, v34
	v_fmamk_f32 v35, v35, 0x44800000, v88
	v_fmamk_f32 v39, v39, 0x44800000, v88
	v_fmamk_f32 v43, v43, 0x44800000, v88
	v_fmamk_f32 v47, v47, 0x44800000, v88
	v_med3_f32 v35, v35, v90, v89
	v_med3_f32 v39, v39, v90, v89
	v_med3_f32 v43, v43, v90, v89
	v_med3_f32 v47, v47, v90, v89
	v_perm_b32 v35, v39, v35, v91
	v_perm_b32 v43, v47, v43, v91
	v_lshl_or_b32 v220, v43, 16, v35
	v_fmamk_f32 v36, v36, 0x44800000, v88
	v_fmamk_f32 v40, v40, 0x44800000, v88
	v_fmamk_f32 v44, v44, 0x44800000, v88
	v_fmamk_f32 v48, v48, 0x44800000, v88
	v_med3_f32 v36, v36, v90, v89
	v_med3_f32 v40, v40, v90, v89
	v_med3_f32 v44, v44, v90, v89
	v_med3_f32 v48, v48, v90, v89
	v_perm_b32 v36, v40, v36, v91
	v_perm_b32 v44, v48, v44, v91
	v_lshl_or_b32 v224, v44, 16, v36
	v_fmamk_f32 v37, v37, 0x44800000, v88
	v_fmamk_f32 v41, v41, 0x44800000, v88
	v_fmamk_f32 v45, v45, 0x44800000, v88
	v_fmamk_f32 v49, v49, 0x44800000, v88
	v_med3_f32 v37, v37, v90, v89
	v_med3_f32 v41, v41, v90, v89
	v_med3_f32 v45, v45, v90, v89
	v_med3_f32 v49, v49, v90, v89
	v_perm_b32 v37, v41, v37, v91
	v_perm_b32 v45, v49, v45, v91
	v_lshl_or_b32 v228, v45, 16, v37
	s_waitcnt vmcnt(0)
	v_fmamk_f32 v50, v50, 0x44800000, v88
	v_fmamk_f32 v54, v54, 0x44800000, v88
	v_fmamk_f32 v58, v58, 0x44800000, v88
	v_fmamk_f32 v62, v62, 0x44800000, v88
	v_med3_f32 v50, v50, v90, v89
	v_med3_f32 v54, v54, v90, v89
	v_med3_f32 v58, v58, v90, v89
	v_med3_f32 v62, v62, v90, v89
	v_perm_b32 v50, v54, v50, v91
	v_perm_b32 v58, v62, v58, v91
	v_lshl_or_b32 v69, v58, 16, v50
	v_fmamk_f32 v51, v51, 0x44800000, v88
	v_fmamk_f32 v55, v55, 0x44800000, v88
	v_fmamk_f32 v59, v59, 0x44800000, v88
	v_fmamk_f32 v63, v63, 0x44800000, v88
	v_med3_f32 v51, v51, v90, v89
	v_med3_f32 v55, v55, v90, v89
	v_med3_f32 v59, v59, v90, v89
	v_med3_f32 v63, v63, v90, v89
	v_perm_b32 v51, v55, v51, v91
	v_perm_b32 v59, v63, v59, v91
	v_lshl_or_b32 v221, v59, 16, v51
	v_fmamk_f32 v52, v52, 0x44800000, v88
	v_fmamk_f32 v56, v56, 0x44800000, v88
	v_fmamk_f32 v60, v60, 0x44800000, v88
	v_fmamk_f32 v64, v64, 0x44800000, v88
	v_med3_f32 v52, v52, v90, v89
	v_med3_f32 v56, v56, v90, v89
	v_med3_f32 v60, v60, v90, v89
	v_med3_f32 v64, v64, v90, v89
	v_perm_b32 v52, v56, v52, v91
	v_perm_b32 v60, v64, v60, v91
	v_lshl_or_b32 v225, v60, 16, v52
	v_fmamk_f32 v53, v53, 0x44800000, v88
	v_fmamk_f32 v57, v57, 0x44800000, v88
	v_fmamk_f32 v61, v61, 0x44800000, v88
	v_fmamk_f32 v65, v65, 0x44800000, v88
	v_med3_f32 v53, v53, v90, v89
	v_med3_f32 v57, v57, v90, v89
	v_med3_f32 v61, v61, v90, v89
	v_med3_f32 v65, v65, v90, v89
	v_perm_b32 v53, v57, v53, v91
	v_perm_b32 v61, v65, v61, v91
	v_lshl_or_b32 v229, v61, 16, v53
	ds_write_b128 v72, v[66:69]
	ds_write_b128 v72, v[218:221] offset:528
	ds_write_b128 v72, v[222:225] offset:1056
	ds_write_b128 v72, v[226:229] offset:1584
	s_mov_b64 s[28:29], 0

.LBB0_538:
	s_mov_b32 s19, s20
	s_mov_b32 s10, s84
	s_mov_b32 s78, s21
	s_mov_b32 s69, s13
	s_mov_b32 s12, s18
	s_mov_b32 s68, s11
	s_mov_b64 s[80:81], s[82:83]
	s_mov_b64 s[30:31], -1
	s_mov_b64 s[2:3], 0
	s_cmp_lt_i32 s20, 2
	s_mov_b64 s[28:29], 0
	s_cbranch_scc1 .LBB0_545
	s_cmp_eq_u32 s19, 2
	s_mov_b64 s[28:29], -1
	s_cbranch_scc0 .LBB0_541
	s_waitcnt vmcnt(12)
	v_mov_b32_e32 v77, 0x4b400000
	v_mov_b32_e32 v79, 0x4b40007f
	v_mov_b32_e32 v82, 0x4b3fff81
	v_mov_b32_e32 v83, 0xc0c0400
	v_add_u32_e32 v74, v199, v198
	v_fmamk_f32 v2, v2, 0x44800000, v77
	v_fmamk_f32 v6, v6, 0x44800000, v77
	v_fmamk_f32 v10, v10, 0x44800000, v77
	v_fmamk_f32 v14, v14, 0x44800000, v77
	v_med3_f32 v2, v2, v82, v79
	v_med3_f32 v6, v6, v82, v79
	v_med3_f32 v10, v10, v82, v79
	v_med3_f32 v14, v14, v82, v79
	v_perm_b32 v2, v6, v2, v83
	v_perm_b32 v10, v14, v10, v83
	v_lshl_or_b32 v66, v10, 16, v2
	v_fmamk_f32 v3, v3, 0x44800000, v77
	v_fmamk_f32 v7, v7, 0x44800000, v77
	v_fmamk_f32 v11, v11, 0x44800000, v77
	v_fmamk_f32 v15, v15, 0x44800000, v77
	v_med3_f32 v3, v3, v82, v79
	v_med3_f32 v7, v7, v82, v79
	v_med3_f32 v11, v11, v82, v79
	v_med3_f32 v15, v15, v82, v79
	v_perm_b32 v3, v7, v3, v83
	v_perm_b32 v11, v15, v11, v83
	v_lshl_or_b32 v218, v11, 16, v3
	v_fmamk_f32 v4, v4, 0x44800000, v77
	v_fmamk_f32 v8, v8, 0x44800000, v77
	v_fmamk_f32 v12, v12, 0x44800000, v77
	v_fmamk_f32 v16, v16, 0x44800000, v77
	v_med3_f32 v4, v4, v82, v79
	v_med3_f32 v8, v8, v82, v79
	v_med3_f32 v12, v12, v82, v79
	v_med3_f32 v16, v16, v82, v79
	v_perm_b32 v4, v8, v4, v83
	v_perm_b32 v12, v16, v12, v83
	v_lshl_or_b32 v222, v12, 16, v4
	v_fmamk_f32 v5, v5, 0x44800000, v77
	v_fmamk_f32 v9, v9, 0x44800000, v77
	v_fmamk_f32 v13, v13, 0x44800000, v77
	v_fmamk_f32 v17, v17, 0x44800000, v77
	v_med3_f32 v5, v5, v82, v79
	v_med3_f32 v9, v9, v82, v79
	v_med3_f32 v13, v13, v82, v79
	v_med3_f32 v17, v17, v82, v79
	v_perm_b32 v5, v9, v5, v83
	v_perm_b32 v13, v17, v13, v83
	v_lshl_or_b32 v226, v13, 16, v5
	s_waitcnt vmcnt(8)
	v_fmamk_f32 v18, v18, 0x44800000, v77
	v_fmamk_f32 v22, v22, 0x44800000, v77
	v_fmamk_f32 v26, v26, 0x44800000, v77
	v_fmamk_f32 v30, v30, 0x44800000, v77
	v_med3_f32 v18, v18, v82, v79
	v_med3_f32 v22, v22, v82, v79
	v_med3_f32 v26, v26, v82, v79
	v_med3_f32 v30, v30, v82, v79
	v_perm_b32 v18, v22, v18, v83
	v_perm_b32 v26, v30, v26, v83
	v_lshl_or_b32 v67, v26, 16, v18
	v_fmamk_f32 v19, v19, 0x44800000, v77
	v_fmamk_f32 v23, v23, 0x44800000, v77
	v_fmamk_f32 v27, v27, 0x44800000, v77
	v_fmamk_f32 v31, v31, 0x44800000, v77
	v_med3_f32 v19, v19, v82, v79
	v_med3_f32 v23, v23, v82, v79
	v_med3_f32 v27, v27, v82, v79
	v_med3_f32 v31, v31, v82, v79
	v_perm_b32 v19, v23, v19, v83
	v_perm_b32 v27, v31, v27, v83
	v_lshl_or_b32 v219, v27, 16, v19
	v_fmamk_f32 v20, v20, 0x44800000, v77
	v_fmamk_f32 v24, v24, 0x44800000, v77
	v_fmamk_f32 v28, v28, 0x44800000, v77
	v_fmamk_f32 v32, v32, 0x44800000, v77
	v_med3_f32 v20, v20, v82, v79
	v_med3_f32 v24, v24, v82, v79
	v_med3_f32 v28, v28, v82, v79
	v_med3_f32 v32, v32, v82, v79
	v_perm_b32 v20, v24, v20, v83
	v_perm_b32 v28, v32, v28, v83
	v_lshl_or_b32 v223, v28, 16, v20
	v_fmamk_f32 v21, v21, 0x44800000, v77
	v_fmamk_f32 v25, v25, 0x44800000, v77
	v_fmamk_f32 v29, v29, 0x44800000, v77
	v_fmamk_f32 v33, v33, 0x44800000, v77
	v_med3_f32 v21, v21, v82, v79
	v_med3_f32 v25, v25, v82, v79
	v_med3_f32 v29, v29, v82, v79
	v_med3_f32 v33, v33, v82, v79
	v_perm_b32 v21, v25, v21, v83
	v_perm_b32 v29, v33, v29, v83
	v_lshl_or_b32 v227, v29, 16, v21
	s_waitcnt vmcnt(4)
	v_fmamk_f32 v34, v34, 0x44800000, v77
	v_fmamk_f32 v38, v38, 0x44800000, v77
	v_fmamk_f32 v42, v42, 0x44800000, v77
	v_fmamk_f32 v46, v46, 0x44800000, v77
	v_med3_f32 v34, v34, v82, v79
	v_med3_f32 v38, v38, v82, v79
	v_med3_f32 v42, v42, v82, v79
	v_med3_f32 v46, v46, v82, v79
	v_perm_b32 v34, v38, v34, v83
	v_perm_b32 v42, v46, v42, v83
	v_lshl_or_b32 v68, v42, 16, v34
	v_fmamk_f32 v35, v35, 0x44800000, v77
	v_fmamk_f32 v39, v39, 0x44800000, v77
	v_fmamk_f32 v43, v43, 0x44800000, v77
	v_fmamk_f32 v47, v47, 0x44800000, v77
	v_med3_f32 v35, v35, v82, v79
	v_med3_f32 v39, v39, v82, v79
	v_med3_f32 v43, v43, v82, v79
	v_med3_f32 v47, v47, v82, v79
	v_perm_b32 v35, v39, v35, v83
	v_perm_b32 v43, v47, v43, v83
	v_lshl_or_b32 v220, v43, 16, v35
	v_fmamk_f32 v36, v36, 0x44800000, v77
	v_fmamk_f32 v40, v40, 0x44800000, v77
	v_fmamk_f32 v44, v44, 0x44800000, v77
	v_fmamk_f32 v48, v48, 0x44800000, v77
	v_med3_f32 v36, v36, v82, v79
	v_med3_f32 v40, v40, v82, v79
	v_med3_f32 v44, v44, v82, v79
	v_med3_f32 v48, v48, v82, v79
	v_perm_b32 v36, v40, v36, v83
	v_perm_b32 v44, v48, v44, v83
	v_lshl_or_b32 v224, v44, 16, v36
	v_fmamk_f32 v37, v37, 0x44800000, v77
	v_fmamk_f32 v41, v41, 0x44800000, v77
	v_fmamk_f32 v45, v45, 0x44800000, v77
	v_fmamk_f32 v49, v49, 0x44800000, v77
	v_med3_f32 v37, v37, v82, v79
	v_med3_f32 v41, v41, v82, v79
	v_med3_f32 v45, v45, v82, v79
	v_med3_f32 v49, v49, v82, v79
	v_perm_b32 v37, v41, v37, v83
	v_perm_b32 v45, v49, v45, v83
	v_lshl_or_b32 v228, v45, 16, v37
	s_waitcnt vmcnt(0)
	v_fmamk_f32 v50, v50, 0x44800000, v77
	v_fmamk_f32 v54, v54, 0x44800000, v77
	v_fmamk_f32 v58, v58, 0x44800000, v77
	v_fmamk_f32 v62, v62, 0x44800000, v77
	v_med3_f32 v50, v50, v82, v79
	v_med3_f32 v54, v54, v82, v79
	v_med3_f32 v58, v58, v82, v79
	v_med3_f32 v62, v62, v82, v79
	v_perm_b32 v50, v54, v50, v83
	v_perm_b32 v58, v62, v58, v83
	v_lshl_or_b32 v69, v58, 16, v50
	v_fmamk_f32 v51, v51, 0x44800000, v77
	v_fmamk_f32 v55, v55, 0x44800000, v77
	v_fmamk_f32 v59, v59, 0x44800000, v77
	v_fmamk_f32 v63, v63, 0x44800000, v77
	v_med3_f32 v51, v51, v82, v79
	v_med3_f32 v55, v55, v82, v79
	v_med3_f32 v59, v59, v82, v79
	v_med3_f32 v63, v63, v82, v79
	v_perm_b32 v51, v55, v51, v83
	v_perm_b32 v59, v63, v59, v83
	v_lshl_or_b32 v221, v59, 16, v51
	v_fmamk_f32 v52, v52, 0x44800000, v77
	v_fmamk_f32 v56, v56, 0x44800000, v77
	v_fmamk_f32 v60, v60, 0x44800000, v77
	v_fmamk_f32 v64, v64, 0x44800000, v77
	v_med3_f32 v52, v52, v82, v79
	v_med3_f32 v56, v56, v82, v79
	v_med3_f32 v60, v60, v82, v79
	v_med3_f32 v64, v64, v82, v79
	v_perm_b32 v52, v56, v52, v83
	v_perm_b32 v60, v64, v60, v83
	v_lshl_or_b32 v225, v60, 16, v52
	v_fmamk_f32 v53, v53, 0x44800000, v77
	v_fmamk_f32 v57, v57, 0x44800000, v77
	v_fmamk_f32 v61, v61, 0x44800000, v77
	v_fmamk_f32 v65, v65, 0x44800000, v77
	v_med3_f32 v53, v53, v82, v79
	v_med3_f32 v57, v57, v82, v79
	v_med3_f32 v61, v61, v82, v79
	v_med3_f32 v65, v65, v82, v79
	v_perm_b32 v53, v57, v53, v83
	v_perm_b32 v61, v65, v61, v83
	v_lshl_or_b32 v229, v61, 16, v53
	ds_write_b128 v74, v[66:69]
	ds_write_b128 v74, v[218:221] offset:528
	ds_write_b128 v74, v[222:225] offset:1056
	ds_write_b128 v74, v[226:229] offset:1584
	s_mov_b64 s[28:29], 0

.LBB0_779:
	v_readlane_b32 s36, v254, 38
	s_mov_b32 s19, s20
	s_mov_b32 s10, s82
	s_mov_b32 s74, s21
	s_mov_b32 s67, s13
	s_mov_b32 s12, s18
	s_mov_b32 s66, s11
	s_mov_b64 s[78:79], s[80:81]
	s_mov_b64 s[30:31], -1
	s_mov_b64 s[2:3], 0
	s_cmp_lt_i32 s20, 2
	s_mov_b64 s[28:29], 0
	v_readlane_b32 s50, v254, 52
	v_readlane_b32 s51, v254, 53
	v_readlane_b32 s37, v254, 39
	v_readlane_b32 s38, v254, 40
	v_readlane_b32 s39, v254, 41
	v_readlane_b32 s40, v254, 42
	v_readlane_b32 s41, v254, 43
	v_readlane_b32 s42, v254, 44
	v_readlane_b32 s43, v254, 45
	v_readlane_b32 s44, v254, 46
	v_readlane_b32 s45, v254, 47
	v_readlane_b32 s46, v254, 48
	v_readlane_b32 s47, v254, 49
	v_readlane_b32 s48, v254, 50
	v_readlane_b32 s49, v254, 51
	s_cbranch_scc1 .LBB0_786
	s_cmp_eq_u32 s19, 2
	s_mov_b64 s[28:29], -1
	s_cbranch_scc0 .LBB0_782
	s_waitcnt vmcnt(12)
	v_mov_b32_e32 v73, 0x4b400000
	v_mov_b32_e32 v74, 0x4b40007f
	v_mov_b32_e32 v75, 0x4b3fff81
	v_mov_b32_e32 v76, 0xc0c0400
	v_add_u32_e32 v70, v199, v198
	v_fmamk_f32 v2, v2, 0x44800000, v73
	v_fmamk_f32 v6, v6, 0x44800000, v73
	v_fmamk_f32 v10, v10, 0x44800000, v73
	v_fmamk_f32 v14, v14, 0x44800000, v73
	v_med3_f32 v2, v2, v75, v74
	v_med3_f32 v6, v6, v75, v74
	v_med3_f32 v10, v10, v75, v74
	v_med3_f32 v14, v14, v75, v74
	v_perm_b32 v2, v6, v2, v76
	v_perm_b32 v10, v14, v10, v76
	v_lshl_or_b32 v66, v10, 16, v2
	v_fmamk_f32 v3, v3, 0x44800000, v73
	v_fmamk_f32 v7, v7, 0x44800000, v73
	v_fmamk_f32 v11, v11, 0x44800000, v73
	v_fmamk_f32 v15, v15, 0x44800000, v73
	v_med3_f32 v3, v3, v75, v74
	v_med3_f32 v7, v7, v75, v74
	v_med3_f32 v11, v11, v75, v74
	v_med3_f32 v15, v15, v75, v74
	v_perm_b32 v3, v7, v3, v76
	v_perm_b32 v11, v15, v11, v76
	v_lshl_or_b32 v218, v11, 16, v3
	v_fmamk_f32 v4, v4, 0x44800000, v73
	v_fmamk_f32 v8, v8, 0x44800000, v73
	v_fmamk_f32 v12, v12, 0x44800000, v73
	v_fmamk_f32 v16, v16, 0x44800000, v73
	v_med3_f32 v4, v4, v75, v74
	v_med3_f32 v8, v8, v75, v74
	v_med3_f32 v12, v12, v75, v74
	v_med3_f32 v16, v16, v75, v74
	v_perm_b32 v4, v8, v4, v76
	v_perm_b32 v12, v16, v12, v76
	v_lshl_or_b32 v222, v12, 16, v4
	v_fmamk_f32 v5, v5, 0x44800000, v73
	v_fmamk_f32 v9, v9, 0x44800000, v73
	v_fmamk_f32 v13, v13, 0x44800000, v73
	v_fmamk_f32 v17, v17, 0x44800000, v73
	v_med3_f32 v5, v5, v75, v74
	v_med3_f32 v9, v9, v75, v74
	v_med3_f32 v13, v13, v75, v74
	v_med3_f32 v17, v17, v75, v74
	v_perm_b32 v5, v9, v5, v76
	v_perm_b32 v13, v17, v13, v76
	v_lshl_or_b32 v226, v13, 16, v5
	s_waitcnt vmcnt(8)
	v_fmamk_f32 v18, v18, 0x44800000, v73
	v_fmamk_f32 v22, v22, 0x44800000, v73
	v_fmamk_f32 v26, v26, 0x44800000, v73
	v_fmamk_f32 v30, v30, 0x44800000, v73
	v_med3_f32 v18, v18, v75, v74
	v_med3_f32 v22, v22, v75, v74
	v_med3_f32 v26, v26, v75, v74
	v_med3_f32 v30, v30, v75, v74
	v_perm_b32 v18, v22, v18, v76
	v_perm_b32 v26, v30, v26, v76
	v_lshl_or_b32 v67, v26, 16, v18
	v_fmamk_f32 v19, v19, 0x44800000, v73
	v_fmamk_f32 v23, v23, 0x44800000, v73
	v_fmamk_f32 v27, v27, 0x44800000, v73
	v_fmamk_f32 v31, v31, 0x44800000, v73
	v_med3_f32 v19, v19, v75, v74
	v_med3_f32 v23, v23, v75, v74
	v_med3_f32 v27, v27, v75, v74
	v_med3_f32 v31, v31, v75, v74
	v_perm_b32 v19, v23, v19, v76
	v_perm_b32 v27, v31, v27, v76
	v_lshl_or_b32 v219, v27, 16, v19
	v_fmamk_f32 v20, v20, 0x44800000, v73
	v_fmamk_f32 v24, v24, 0x44800000, v73
	v_fmamk_f32 v28, v28, 0x44800000, v73
	v_fmamk_f32 v32, v32, 0x44800000, v73
	v_med3_f32 v20, v20, v75, v74
	v_med3_f32 v24, v24, v75, v74
	v_med3_f32 v28, v28, v75, v74
	v_med3_f32 v32, v32, v75, v74
	v_perm_b32 v20, v24, v20, v76
	v_perm_b32 v28, v32, v28, v76
	v_lshl_or_b32 v223, v28, 16, v20
	v_fmamk_f32 v21, v21, 0x44800000, v73
	v_fmamk_f32 v25, v25, 0x44800000, v73
	v_fmamk_f32 v29, v29, 0x44800000, v73
	v_fmamk_f32 v33, v33, 0x44800000, v73
	v_med3_f32 v21, v21, v75, v74
	v_med3_f32 v25, v25, v75, v74
	v_med3_f32 v29, v29, v75, v74
	v_med3_f32 v33, v33, v75, v74
	v_perm_b32 v21, v25, v21, v76
	v_perm_b32 v29, v33, v29, v76
	v_lshl_or_b32 v227, v29, 16, v21
	s_waitcnt vmcnt(4)
	v_fmamk_f32 v34, v34, 0x44800000, v73
	v_fmamk_f32 v38, v38, 0x44800000, v73
	v_fmamk_f32 v42, v42, 0x44800000, v73
	v_fmamk_f32 v46, v46, 0x44800000, v73
	v_med3_f32 v34, v34, v75, v74
	v_med3_f32 v38, v38, v75, v74
	v_med3_f32 v42, v42, v75, v74
	v_med3_f32 v46, v46, v75, v74
	v_perm_b32 v34, v38, v34, v76
	v_perm_b32 v42, v46, v42, v76
	v_lshl_or_b32 v68, v42, 16, v34
	v_fmamk_f32 v35, v35, 0x44800000, v73
	v_fmamk_f32 v39, v39, 0x44800000, v73
	v_fmamk_f32 v43, v43, 0x44800000, v73
	v_fmamk_f32 v47, v47, 0x44800000, v73
	v_med3_f32 v35, v35, v75, v74
	v_med3_f32 v39, v39, v75, v74
	v_med3_f32 v43, v43, v75, v74
	v_med3_f32 v47, v47, v75, v74
	v_perm_b32 v35, v39, v35, v76
	v_perm_b32 v43, v47, v43, v76
	v_lshl_or_b32 v220, v43, 16, v35
	v_fmamk_f32 v36, v36, 0x44800000, v73
	v_fmamk_f32 v40, v40, 0x44800000, v73
	v_fmamk_f32 v44, v44, 0x44800000, v73
	v_fmamk_f32 v48, v48, 0x44800000, v73
	v_med3_f32 v36, v36, v75, v74
	v_med3_f32 v40, v40, v75, v74
	v_med3_f32 v44, v44, v75, v74
	v_med3_f32 v48, v48, v75, v74
	v_perm_b32 v36, v40, v36, v76
	v_perm_b32 v44, v48, v44, v76
	v_lshl_or_b32 v224, v44, 16, v36
	v_fmamk_f32 v37, v37, 0x44800000, v73
	v_fmamk_f32 v41, v41, 0x44800000, v73
	v_fmamk_f32 v45, v45, 0x44800000, v73
	v_fmamk_f32 v49, v49, 0x44800000, v73
	v_med3_f32 v37, v37, v75, v74
	v_med3_f32 v41, v41, v75, v74
	v_med3_f32 v45, v45, v75, v74
	v_med3_f32 v49, v49, v75, v74
	v_perm_b32 v37, v41, v37, v76
	v_perm_b32 v45, v49, v45, v76
	v_lshl_or_b32 v228, v45, 16, v37
	s_waitcnt vmcnt(0)
	v_fmamk_f32 v50, v50, 0x44800000, v73
	v_fmamk_f32 v54, v54, 0x44800000, v73
	v_fmamk_f32 v58, v58, 0x44800000, v73
	v_fmamk_f32 v62, v62, 0x44800000, v73
	v_med3_f32 v50, v50, v75, v74
	v_med3_f32 v54, v54, v75, v74
	v_med3_f32 v58, v58, v75, v74
	v_med3_f32 v62, v62, v75, v74
	v_perm_b32 v50, v54, v50, v76
	v_perm_b32 v58, v62, v58, v76
	v_lshl_or_b32 v69, v58, 16, v50
	v_fmamk_f32 v51, v51, 0x44800000, v73
	v_fmamk_f32 v55, v55, 0x44800000, v73
	v_fmamk_f32 v59, v59, 0x44800000, v73
	v_fmamk_f32 v63, v63, 0x44800000, v73
	v_med3_f32 v51, v51, v75, v74
	v_med3_f32 v55, v55, v75, v74
	v_med3_f32 v59, v59, v75, v74
	v_med3_f32 v63, v63, v75, v74
	v_perm_b32 v51, v55, v51, v76
	v_perm_b32 v59, v63, v59, v76
	v_lshl_or_b32 v221, v59, 16, v51
	v_fmamk_f32 v52, v52, 0x44800000, v73
	v_fmamk_f32 v56, v56, 0x44800000, v73
	v_fmamk_f32 v60, v60, 0x44800000, v73
	v_fmamk_f32 v64, v64, 0x44800000, v73
	v_med3_f32 v52, v52, v75, v74
	v_med3_f32 v56, v56, v75, v74
	v_med3_f32 v60, v60, v75, v74
	v_med3_f32 v64, v64, v75, v74
	v_perm_b32 v52, v56, v52, v76
	v_perm_b32 v60, v64, v60, v76
	v_lshl_or_b32 v225, v60, 16, v52
	v_fmamk_f32 v53, v53, 0x44800000, v73
	v_fmamk_f32 v57, v57, 0x44800000, v73
	v_fmamk_f32 v61, v61, 0x44800000, v73
	v_fmamk_f32 v65, v65, 0x44800000, v73
	v_med3_f32 v53, v53, v75, v74
	v_med3_f32 v57, v57, v75, v74
	v_med3_f32 v61, v61, v75, v74
	v_med3_f32 v65, v65, v75, v74
	v_perm_b32 v53, v57, v53, v76
	v_perm_b32 v61, v65, v61, v76
	v_lshl_or_b32 v229, v61, 16, v53
	ds_write_b128 v70, v[66:69]
	ds_write_b128 v70, v[218:221] offset:528
	ds_write_b128 v70, v[222:225] offset:1056
	ds_write_b128 v70, v[226:229] offset:1584
	s_mov_b64 s[28:29], 0

.LBB0_1073:
	v_readlane_b32 s36, v254, 38
	s_mov_b32 s22, s21
	s_mov_b32 s13, s82
	s_mov_b32 s74, s23
	s_mov_b32 s11, s19
	s_mov_b32 s12, s20
	s_mov_b32 s10, s18
	s_mov_b64 s[78:79], s[80:81]
	s_mov_b64 s[30:31], -1
	s_mov_b64 s[2:3], 0
	s_cmp_lt_i32 s21, 2
	s_mov_b64 s[28:29], 0
	v_readlane_b32 s50, v254, 52
	v_readlane_b32 s51, v254, 53
	v_readlane_b32 s37, v254, 39
	v_readlane_b32 s38, v254, 40
	v_readlane_b32 s39, v254, 41
	v_readlane_b32 s40, v254, 42
	v_readlane_b32 s41, v254, 43
	v_readlane_b32 s42, v254, 44
	v_readlane_b32 s43, v254, 45
	v_readlane_b32 s44, v254, 46
	v_readlane_b32 s45, v254, 47
	v_readlane_b32 s46, v254, 48
	v_readlane_b32 s47, v254, 49
	v_readlane_b32 s48, v254, 50
	v_readlane_b32 s49, v254, 51
	s_cbranch_scc1 .LBB0_1080
	s_cmp_eq_u32 s22, 2
	s_mov_b64 s[28:29], -1
	s_cbranch_scc0 .LBB0_1076
	s_waitcnt vmcnt(12)
	v_mov_b32_e32 v73, 0x4b400000
	v_mov_b32_e32 v74, 0x4b40007f
	v_mov_b32_e32 v75, 0x4b3fff81
	v_mov_b32_e32 v76, 0xc0c0400
	v_add_u32_e32 v70, v199, v198
	v_fmamk_f32 v2, v2, 0x44800000, v73
	v_fmamk_f32 v6, v6, 0x44800000, v73
	v_fmamk_f32 v10, v10, 0x44800000, v73
	v_fmamk_f32 v14, v14, 0x44800000, v73
	v_med3_f32 v2, v2, v75, v74
	v_med3_f32 v6, v6, v75, v74
	v_med3_f32 v10, v10, v75, v74
	v_med3_f32 v14, v14, v75, v74
	v_perm_b32 v2, v6, v2, v76
	v_perm_b32 v10, v14, v10, v76
	v_lshl_or_b32 v66, v10, 16, v2
	v_fmamk_f32 v3, v3, 0x44800000, v73
	v_fmamk_f32 v7, v7, 0x44800000, v73
	v_fmamk_f32 v11, v11, 0x44800000, v73
	v_fmamk_f32 v15, v15, 0x44800000, v73
	v_med3_f32 v3, v3, v75, v74
	v_med3_f32 v7, v7, v75, v74
	v_med3_f32 v11, v11, v75, v74
	v_med3_f32 v15, v15, v75, v74
	v_perm_b32 v3, v7, v3, v76
	v_perm_b32 v11, v15, v11, v76
	v_lshl_or_b32 v218, v11, 16, v3
	v_fmamk_f32 v4, v4, 0x44800000, v73
	v_fmamk_f32 v8, v8, 0x44800000, v73
	v_fmamk_f32 v12, v12, 0x44800000, v73
	v_fmamk_f32 v16, v16, 0x44800000, v73
	v_med3_f32 v4, v4, v75, v74
	v_med3_f32 v8, v8, v75, v74
	v_med3_f32 v12, v12, v75, v74
	v_med3_f32 v16, v16, v75, v74
	v_perm_b32 v4, v8, v4, v76
	v_perm_b32 v12, v16, v12, v76
	v_lshl_or_b32 v222, v12, 16, v4
	v_fmamk_f32 v5, v5, 0x44800000, v73
	v_fmamk_f32 v9, v9, 0x44800000, v73
	v_fmamk_f32 v13, v13, 0x44800000, v73
	v_fmamk_f32 v17, v17, 0x44800000, v73
	v_med3_f32 v5, v5, v75, v74
	v_med3_f32 v9, v9, v75, v74
	v_med3_f32 v13, v13, v75, v74
	v_med3_f32 v17, v17, v75, v74
	v_perm_b32 v5, v9, v5, v76
	v_perm_b32 v13, v17, v13, v76
	v_lshl_or_b32 v226, v13, 16, v5
	s_waitcnt vmcnt(8)
	v_fmamk_f32 v18, v18, 0x44800000, v73
	v_fmamk_f32 v22, v22, 0x44800000, v73
	v_fmamk_f32 v26, v26, 0x44800000, v73
	v_fmamk_f32 v30, v30, 0x44800000, v73
	v_med3_f32 v18, v18, v75, v74
	v_med3_f32 v22, v22, v75, v74
	v_med3_f32 v26, v26, v75, v74
	v_med3_f32 v30, v30, v75, v74
	v_perm_b32 v18, v22, v18, v76
	v_perm_b32 v26, v30, v26, v76
	v_lshl_or_b32 v67, v26, 16, v18
	v_fmamk_f32 v19, v19, 0x44800000, v73
	v_fmamk_f32 v23, v23, 0x44800000, v73
	v_fmamk_f32 v27, v27, 0x44800000, v73
	v_fmamk_f32 v31, v31, 0x44800000, v73
	v_med3_f32 v19, v19, v75, v74
	v_med3_f32 v23, v23, v75, v74
	v_med3_f32 v27, v27, v75, v74
	v_med3_f32 v31, v31, v75, v74
	v_perm_b32 v19, v23, v19, v76
	v_perm_b32 v27, v31, v27, v76
	v_lshl_or_b32 v219, v27, 16, v19
	v_fmamk_f32 v20, v20, 0x44800000, v73
	v_fmamk_f32 v24, v24, 0x44800000, v73
	v_fmamk_f32 v28, v28, 0x44800000, v73
	v_fmamk_f32 v32, v32, 0x44800000, v73
	v_med3_f32 v20, v20, v75, v74
	v_med3_f32 v24, v24, v75, v74
	v_med3_f32 v28, v28, v75, v74
	v_med3_f32 v32, v32, v75, v74
	v_perm_b32 v20, v24, v20, v76
	v_perm_b32 v28, v32, v28, v76
	v_lshl_or_b32 v223, v28, 16, v20
	v_fmamk_f32 v21, v21, 0x44800000, v73
	v_fmamk_f32 v25, v25, 0x44800000, v73
	v_fmamk_f32 v29, v29, 0x44800000, v73
	v_fmamk_f32 v33, v33, 0x44800000, v73
	v_med3_f32 v21, v21, v75, v74
	v_med3_f32 v25, v25, v75, v74
	v_med3_f32 v29, v29, v75, v74
	v_med3_f32 v33, v33, v75, v74
	v_perm_b32 v21, v25, v21, v76
	v_perm_b32 v29, v33, v29, v76
	v_lshl_or_b32 v227, v29, 16, v21
	s_waitcnt vmcnt(4)
	v_fmamk_f32 v34, v34, 0x44800000, v73
	v_fmamk_f32 v38, v38, 0x44800000, v73
	v_fmamk_f32 v42, v42, 0x44800000, v73
	v_fmamk_f32 v46, v46, 0x44800000, v73
	v_med3_f32 v34, v34, v75, v74
	v_med3_f32 v38, v38, v75, v74
	v_med3_f32 v42, v42, v75, v74
	v_med3_f32 v46, v46, v75, v74
	v_perm_b32 v34, v38, v34, v76
	v_perm_b32 v42, v46, v42, v76
	v_lshl_or_b32 v68, v42, 16, v34
	v_fmamk_f32 v35, v35, 0x44800000, v73
	v_fmamk_f32 v39, v39, 0x44800000, v73
	v_fmamk_f32 v43, v43, 0x44800000, v73
	v_fmamk_f32 v47, v47, 0x44800000, v73
	v_med3_f32 v35, v35, v75, v74
	v_med3_f32 v39, v39, v75, v74
	v_med3_f32 v43, v43, v75, v74
	v_med3_f32 v47, v47, v75, v74
	v_perm_b32 v35, v39, v35, v76
	v_perm_b32 v43, v47, v43, v76
	v_lshl_or_b32 v220, v43, 16, v35
	v_fmamk_f32 v36, v36, 0x44800000, v73
	v_fmamk_f32 v40, v40, 0x44800000, v73
	v_fmamk_f32 v44, v44, 0x44800000, v73
	v_fmamk_f32 v48, v48, 0x44800000, v73
	v_med3_f32 v36, v36, v75, v74
	v_med3_f32 v40, v40, v75, v74
	v_med3_f32 v44, v44, v75, v74
	v_med3_f32 v48, v48, v75, v74
	v_perm_b32 v36, v40, v36, v76
	v_perm_b32 v44, v48, v44, v76
	v_lshl_or_b32 v224, v44, 16, v36
	v_fmamk_f32 v37, v37, 0x44800000, v73
	v_fmamk_f32 v41, v41, 0x44800000, v73
	v_fmamk_f32 v45, v45, 0x44800000, v73
	v_fmamk_f32 v49, v49, 0x44800000, v73
	v_med3_f32 v37, v37, v75, v74
	v_med3_f32 v41, v41, v75, v74
	v_med3_f32 v45, v45, v75, v74
	v_med3_f32 v49, v49, v75, v74
	v_perm_b32 v37, v41, v37, v76
	v_perm_b32 v45, v49, v45, v76
	v_lshl_or_b32 v228, v45, 16, v37
	s_waitcnt vmcnt(0)
	v_fmamk_f32 v50, v50, 0x44800000, v73
	v_fmamk_f32 v54, v54, 0x44800000, v73
	v_fmamk_f32 v58, v58, 0x44800000, v73
	v_fmamk_f32 v62, v62, 0x44800000, v73
	v_med3_f32 v50, v50, v75, v74
	v_med3_f32 v54, v54, v75, v74
	v_med3_f32 v58, v58, v75, v74
	v_med3_f32 v62, v62, v75, v74
	v_perm_b32 v50, v54, v50, v76
	v_perm_b32 v58, v62, v58, v76
	v_lshl_or_b32 v69, v58, 16, v50
	v_fmamk_f32 v51, v51, 0x44800000, v73
	v_fmamk_f32 v55, v55, 0x44800000, v73
	v_fmamk_f32 v59, v59, 0x44800000, v73
	v_fmamk_f32 v63, v63, 0x44800000, v73
	v_med3_f32 v51, v51, v75, v74
	v_med3_f32 v55, v55, v75, v74
	v_med3_f32 v59, v59, v75, v74
	v_med3_f32 v63, v63, v75, v74
	v_perm_b32 v51, v55, v51, v76
	v_perm_b32 v59, v63, v59, v76
	v_lshl_or_b32 v221, v59, 16, v51
	v_fmamk_f32 v52, v52, 0x44800000, v73
	v_fmamk_f32 v56, v56, 0x44800000, v73
	v_fmamk_f32 v60, v60, 0x44800000, v73
	v_fmamk_f32 v64, v64, 0x44800000, v73
	v_med3_f32 v52, v52, v75, v74
	v_med3_f32 v56, v56, v75, v74
	v_med3_f32 v60, v60, v75, v74
	v_med3_f32 v64, v64, v75, v74
	v_perm_b32 v52, v56, v52, v76
	v_perm_b32 v60, v64, v60, v76
	v_lshl_or_b32 v225, v60, 16, v52
	v_fmamk_f32 v53, v53, 0x44800000, v73
	v_fmamk_f32 v57, v57, 0x44800000, v73
	v_fmamk_f32 v61, v61, 0x44800000, v73
	v_fmamk_f32 v65, v65, 0x44800000, v73
	v_med3_f32 v53, v53, v75, v74
	v_med3_f32 v57, v57, v75, v74
	v_med3_f32 v61, v61, v75, v74
	v_med3_f32 v65, v65, v75, v74
	v_perm_b32 v53, v57, v53, v76
	v_perm_b32 v61, v65, v61, v76
	v_lshl_or_b32 v229, v61, 16, v53
	ds_write_b128 v70, v[66:69]
	ds_write_b128 v70, v[218:221] offset:528
	ds_write_b128 v70, v[222:225] offset:1056
	ds_write_b128 v70, v[226:229] offset:1584
	s_mov_b64 s[28:29], 0

.LBB0_1554:
	s_mov_b32 s59, s58
	s_mov_b32 s52, s88
	s_mov_b32 s82, s60
	s_mov_b32 s27, s54
	s_mov_b32 s33, s55
	s_mov_b32 s26, s53
	s_mov_b64 s[84:85], s[86:87]
	s_mov_b64 s[30:31], -1
	s_mov_b64 s[2:3], 0
	s_cmp_lt_i32 s58, 2
	s_mov_b64 s[28:29], 0
	s_cbranch_scc1 .LBB0_1561
	s_cmp_eq_u32 s59, 2
	s_mov_b64 s[28:29], -1
	s_cbranch_scc0 .LBB0_1557
	s_waitcnt vmcnt(12)
	v_mov_b32_e32 v76, 0x4b400000
	v_mov_b32_e32 v77, 0x4b40007f
	v_mov_b32_e32 v90, 0x4b3fff81
	v_mov_b32_e32 v91, 0xc0c0400
	v_add_u32_e32 v89, v79, v78
	v_fmamk_f32 v2, v2, 0x44800000, v76
	v_fmamk_f32 v6, v6, 0x44800000, v76
	v_fmamk_f32 v10, v10, 0x44800000, v76
	v_fmamk_f32 v14, v14, 0x44800000, v76
	v_med3_f32 v2, v2, v90, v77
	v_med3_f32 v6, v6, v90, v77
	v_med3_f32 v10, v10, v90, v77
	v_med3_f32 v14, v14, v90, v77
	v_perm_b32 v2, v6, v2, v91
	v_perm_b32 v10, v14, v10, v91
	v_lshl_or_b32 v66, v10, 16, v2
	v_fmamk_f32 v3, v3, 0x44800000, v76
	v_fmamk_f32 v7, v7, 0x44800000, v76
	v_fmamk_f32 v11, v11, 0x44800000, v76
	v_fmamk_f32 v15, v15, 0x44800000, v76
	v_med3_f32 v3, v3, v90, v77
	v_med3_f32 v7, v7, v90, v77
	v_med3_f32 v11, v11, v90, v77
	v_med3_f32 v15, v15, v90, v77
	v_perm_b32 v3, v7, v3, v91
	v_perm_b32 v11, v15, v11, v91
	v_lshl_or_b32 v218, v11, 16, v3
	v_fmamk_f32 v4, v4, 0x44800000, v76
	v_fmamk_f32 v8, v8, 0x44800000, v76
	v_fmamk_f32 v12, v12, 0x44800000, v76
	v_fmamk_f32 v16, v16, 0x44800000, v76
	v_med3_f32 v4, v4, v90, v77
	v_med3_f32 v8, v8, v90, v77
	v_med3_f32 v12, v12, v90, v77
	v_med3_f32 v16, v16, v90, v77
	v_perm_b32 v4, v8, v4, v91
	v_perm_b32 v12, v16, v12, v91
	v_lshl_or_b32 v222, v12, 16, v4
	v_fmamk_f32 v5, v5, 0x44800000, v76
	v_fmamk_f32 v9, v9, 0x44800000, v76
	v_fmamk_f32 v13, v13, 0x44800000, v76
	v_fmamk_f32 v17, v17, 0x44800000, v76
	v_med3_f32 v5, v5, v90, v77
	v_med3_f32 v9, v9, v90, v77
	v_med3_f32 v13, v13, v90, v77
	v_med3_f32 v17, v17, v90, v77
	v_perm_b32 v5, v9, v5, v91
	v_perm_b32 v13, v17, v13, v91
	v_lshl_or_b32 v226, v13, 16, v5
	s_waitcnt vmcnt(8)
	v_fmamk_f32 v18, v18, 0x44800000, v76
	v_fmamk_f32 v22, v22, 0x44800000, v76
	v_fmamk_f32 v26, v26, 0x44800000, v76
	v_fmamk_f32 v30, v30, 0x44800000, v76
	v_med3_f32 v18, v18, v90, v77
	v_med3_f32 v22, v22, v90, v77
	v_med3_f32 v26, v26, v90, v77
	v_med3_f32 v30, v30, v90, v77
	v_perm_b32 v18, v22, v18, v91
	v_perm_b32 v26, v30, v26, v91
	v_lshl_or_b32 v67, v26, 16, v18
	v_fmamk_f32 v19, v19, 0x44800000, v76
	v_fmamk_f32 v23, v23, 0x44800000, v76
	v_fmamk_f32 v27, v27, 0x44800000, v76
	v_fmamk_f32 v31, v31, 0x44800000, v76
	v_med3_f32 v19, v19, v90, v77
	v_med3_f32 v23, v23, v90, v77
	v_med3_f32 v27, v27, v90, v77
	v_med3_f32 v31, v31, v90, v77
	v_perm_b32 v19, v23, v19, v91
	v_perm_b32 v27, v31, v27, v91
	v_lshl_or_b32 v219, v27, 16, v19
	v_fmamk_f32 v20, v20, 0x44800000, v76
	v_fmamk_f32 v24, v24, 0x44800000, v76
	v_fmamk_f32 v28, v28, 0x44800000, v76
	v_fmamk_f32 v32, v32, 0x44800000, v76
	v_med3_f32 v20, v20, v90, v77
	v_med3_f32 v24, v24, v90, v77
	v_med3_f32 v28, v28, v90, v77
	v_med3_f32 v32, v32, v90, v77
	v_perm_b32 v20, v24, v20, v91
	v_perm_b32 v28, v32, v28, v91
	v_lshl_or_b32 v223, v28, 16, v20
	v_fmamk_f32 v21, v21, 0x44800000, v76
	v_fmamk_f32 v25, v25, 0x44800000, v76
	v_fmamk_f32 v29, v29, 0x44800000, v76
	v_fmamk_f32 v33, v33, 0x44800000, v76
	v_med3_f32 v21, v21, v90, v77
	v_med3_f32 v25, v25, v90, v77
	v_med3_f32 v29, v29, v90, v77
	v_med3_f32 v33, v33, v90, v77
	v_perm_b32 v21, v25, v21, v91
	v_perm_b32 v29, v33, v29, v91
	v_lshl_or_b32 v227, v29, 16, v21
	s_waitcnt vmcnt(4)
	v_fmamk_f32 v34, v34, 0x44800000, v76
	v_fmamk_f32 v38, v38, 0x44800000, v76
	v_fmamk_f32 v42, v42, 0x44800000, v76
	v_fmamk_f32 v46, v46, 0x44800000, v76
	v_med3_f32 v34, v34, v90, v77
	v_med3_f32 v38, v38, v90, v77
	v_med3_f32 v42, v42, v90, v77
	v_med3_f32 v46, v46, v90, v77
	v_perm_b32 v34, v38, v34, v91
	v_perm_b32 v42, v46, v42, v91
	v_lshl_or_b32 v68, v42, 16, v34
	v_fmamk_f32 v35, v35, 0x44800000, v76
	v_fmamk_f32 v39, v39, 0x44800000, v76
	v_fmamk_f32 v43, v43, 0x44800000, v76
	v_fmamk_f32 v47, v47, 0x44800000, v76
	v_med3_f32 v35, v35, v90, v77
	v_med3_f32 v39, v39, v90, v77
	v_med3_f32 v43, v43, v90, v77
	v_med3_f32 v47, v47, v90, v77
	v_perm_b32 v35, v39, v35, v91
	v_perm_b32 v43, v47, v43, v91
	v_lshl_or_b32 v220, v43, 16, v35
	v_fmamk_f32 v36, v36, 0x44800000, v76
	v_fmamk_f32 v40, v40, 0x44800000, v76
	v_fmamk_f32 v44, v44, 0x44800000, v76
	v_fmamk_f32 v48, v48, 0x44800000, v76
	v_med3_f32 v36, v36, v90, v77
	v_med3_f32 v40, v40, v90, v77
	v_med3_f32 v44, v44, v90, v77
	v_med3_f32 v48, v48, v90, v77
	v_perm_b32 v36, v40, v36, v91
	v_perm_b32 v44, v48, v44, v91
	v_lshl_or_b32 v224, v44, 16, v36
	v_fmamk_f32 v37, v37, 0x44800000, v76
	v_fmamk_f32 v41, v41, 0x44800000, v76
	v_fmamk_f32 v45, v45, 0x44800000, v76
	v_fmamk_f32 v49, v49, 0x44800000, v76
	v_med3_f32 v37, v37, v90, v77
	v_med3_f32 v41, v41, v90, v77
	v_med3_f32 v45, v45, v90, v77
	v_med3_f32 v49, v49, v90, v77
	v_perm_b32 v37, v41, v37, v91
	v_perm_b32 v45, v49, v45, v91
	v_lshl_or_b32 v228, v45, 16, v37
	s_waitcnt vmcnt(0)
	v_fmamk_f32 v50, v50, 0x44800000, v76
	v_fmamk_f32 v54, v54, 0x44800000, v76
	v_fmamk_f32 v58, v58, 0x44800000, v76
	v_fmamk_f32 v62, v62, 0x44800000, v76
	v_med3_f32 v50, v50, v90, v77
	v_med3_f32 v54, v54, v90, v77
	v_med3_f32 v58, v58, v90, v77
	v_med3_f32 v62, v62, v90, v77
	v_perm_b32 v50, v54, v50, v91
	v_perm_b32 v58, v62, v58, v91
	v_lshl_or_b32 v69, v58, 16, v50
	v_fmamk_f32 v51, v51, 0x44800000, v76
	v_fmamk_f32 v55, v55, 0x44800000, v76
	v_fmamk_f32 v59, v59, 0x44800000, v76
	v_fmamk_f32 v63, v63, 0x44800000, v76
	v_med3_f32 v51, v51, v90, v77
	v_med3_f32 v55, v55, v90, v77
	v_med3_f32 v59, v59, v90, v77
	v_med3_f32 v63, v63, v90, v77
	v_perm_b32 v51, v55, v51, v91
	v_perm_b32 v59, v63, v59, v91
	v_lshl_or_b32 v221, v59, 16, v51
	v_fmamk_f32 v52, v52, 0x44800000, v76
	v_fmamk_f32 v56, v56, 0x44800000, v76
	v_fmamk_f32 v60, v60, 0x44800000, v76
	v_fmamk_f32 v64, v64, 0x44800000, v76
	v_med3_f32 v52, v52, v90, v77
	v_med3_f32 v56, v56, v90, v77
	v_med3_f32 v60, v60, v90, v77
	v_med3_f32 v64, v64, v90, v77
	v_perm_b32 v52, v56, v52, v91
	v_perm_b32 v60, v64, v60, v91
	v_lshl_or_b32 v225, v60, 16, v52
	v_fmamk_f32 v53, v53, 0x44800000, v76
	v_fmamk_f32 v57, v57, 0x44800000, v76
	v_fmamk_f32 v61, v61, 0x44800000, v76
	v_fmamk_f32 v65, v65, 0x44800000, v76
	v_med3_f32 v53, v53, v90, v77
	v_med3_f32 v57, v57, v90, v77
	v_med3_f32 v61, v61, v90, v77
	v_med3_f32 v65, v65, v90, v77
	v_perm_b32 v53, v57, v53, v91
	v_perm_b32 v61, v65, v61, v91
	v_lshl_or_b32 v229, v61, 16, v53
	ds_write_b128 v89, v[66:69]
	ds_write_b128 v89, v[218:221] offset:528
	ds_write_b128 v89, v[222:225] offset:1056
	ds_write_b128 v89, v[226:229] offset:1584
	s_mov_b64 s[28:29], 0

.LBB0_2106:
	s_mov_b32 s69, s25
	s_mov_b32 s19, s80
	s_mov_b32 s68, s83
	s_mov_b32 s11, s23
	s_mov_b32 s18, s24
	s_mov_b32 s10, s22
	s_mov_b64 s[76:77], s[78:79]
	s_mov_b64 s[30:31], -1
	s_mov_b64 s[2:3], 0
	s_cmp_lt_i32 s25, 2
	s_mov_b64 s[28:29], 0
	s_cbranch_scc1 .LBB0_2113
	s_cmp_eq_u32 s69, 2
	s_mov_b64 s[28:29], -1
	s_cbranch_scc0 .LBB0_2109
	s_waitcnt vmcnt(12)
	v_mov_b32_e32 v77, 0x4b400000
	v_mov_b32_e32 v79, 0x4b40007f
	v_mov_b32_e32 v83, 0x4b3fff81
	v_mov_b32_e32 v84, 0xc0c0400
	v_add_u32_e32 v74, v199, v198
	v_fmamk_f32 v2, v2, 0x44800000, v77
	v_fmamk_f32 v6, v6, 0x44800000, v77
	v_fmamk_f32 v10, v10, 0x44800000, v77
	v_fmamk_f32 v14, v14, 0x44800000, v77
	v_med3_f32 v2, v2, v83, v79
	v_med3_f32 v6, v6, v83, v79
	v_med3_f32 v10, v10, v83, v79
	v_med3_f32 v14, v14, v83, v79
	v_perm_b32 v2, v6, v2, v84
	v_perm_b32 v10, v14, v10, v84
	v_lshl_or_b32 v66, v10, 16, v2
	v_fmamk_f32 v3, v3, 0x44800000, v77
	v_fmamk_f32 v7, v7, 0x44800000, v77
	v_fmamk_f32 v11, v11, 0x44800000, v77
	v_fmamk_f32 v15, v15, 0x44800000, v77
	v_med3_f32 v3, v3, v83, v79
	v_med3_f32 v7, v7, v83, v79
	v_med3_f32 v11, v11, v83, v79
	v_med3_f32 v15, v15, v83, v79
	v_perm_b32 v3, v7, v3, v84
	v_perm_b32 v11, v15, v11, v84
	v_lshl_or_b32 v218, v11, 16, v3
	v_fmamk_f32 v4, v4, 0x44800000, v77
	v_fmamk_f32 v8, v8, 0x44800000, v77
	v_fmamk_f32 v12, v12, 0x44800000, v77
	v_fmamk_f32 v16, v16, 0x44800000, v77
	v_med3_f32 v4, v4, v83, v79
	v_med3_f32 v8, v8, v83, v79
	v_med3_f32 v12, v12, v83, v79
	v_med3_f32 v16, v16, v83, v79
	v_perm_b32 v4, v8, v4, v84
	v_perm_b32 v12, v16, v12, v84
	v_lshl_or_b32 v222, v12, 16, v4
	v_fmamk_f32 v5, v5, 0x44800000, v77
	v_fmamk_f32 v9, v9, 0x44800000, v77
	v_fmamk_f32 v13, v13, 0x44800000, v77
	v_fmamk_f32 v17, v17, 0x44800000, v77
	v_med3_f32 v5, v5, v83, v79
	v_med3_f32 v9, v9, v83, v79
	v_med3_f32 v13, v13, v83, v79
	v_med3_f32 v17, v17, v83, v79
	v_perm_b32 v5, v9, v5, v84
	v_perm_b32 v13, v17, v13, v84
	v_lshl_or_b32 v226, v13, 16, v5
	s_waitcnt vmcnt(8)
	v_fmamk_f32 v18, v18, 0x44800000, v77
	v_fmamk_f32 v22, v22, 0x44800000, v77
	v_fmamk_f32 v26, v26, 0x44800000, v77
	v_fmamk_f32 v30, v30, 0x44800000, v77
	v_med3_f32 v18, v18, v83, v79
	v_med3_f32 v22, v22, v83, v79
	v_med3_f32 v26, v26, v83, v79
	v_med3_f32 v30, v30, v83, v79
	v_perm_b32 v18, v22, v18, v84
	v_perm_b32 v26, v30, v26, v84
	v_lshl_or_b32 v67, v26, 16, v18
	v_fmamk_f32 v19, v19, 0x44800000, v77
	v_fmamk_f32 v23, v23, 0x44800000, v77
	v_fmamk_f32 v27, v27, 0x44800000, v77
	v_fmamk_f32 v31, v31, 0x44800000, v77
	v_med3_f32 v19, v19, v83, v79
	v_med3_f32 v23, v23, v83, v79
	v_med3_f32 v27, v27, v83, v79
	v_med3_f32 v31, v31, v83, v79
	v_perm_b32 v19, v23, v19, v84
	v_perm_b32 v27, v31, v27, v84
	v_lshl_or_b32 v219, v27, 16, v19
	v_fmamk_f32 v20, v20, 0x44800000, v77
	v_fmamk_f32 v24, v24, 0x44800000, v77
	v_fmamk_f32 v28, v28, 0x44800000, v77
	v_fmamk_f32 v32, v32, 0x44800000, v77
	v_med3_f32 v20, v20, v83, v79
	v_med3_f32 v24, v24, v83, v79
	v_med3_f32 v28, v28, v83, v79
	v_med3_f32 v32, v32, v83, v79
	v_perm_b32 v20, v24, v20, v84
	v_perm_b32 v28, v32, v28, v84
	v_lshl_or_b32 v223, v28, 16, v20
	v_fmamk_f32 v21, v21, 0x44800000, v77
	v_fmamk_f32 v25, v25, 0x44800000, v77
	v_fmamk_f32 v29, v29, 0x44800000, v77
	v_fmamk_f32 v33, v33, 0x44800000, v77
	v_med3_f32 v21, v21, v83, v79
	v_med3_f32 v25, v25, v83, v79
	v_med3_f32 v29, v29, v83, v79
	v_med3_f32 v33, v33, v83, v79
	v_perm_b32 v21, v25, v21, v84
	v_perm_b32 v29, v33, v29, v84
	v_lshl_or_b32 v227, v29, 16, v21
	s_waitcnt vmcnt(4)
	v_fmamk_f32 v34, v34, 0x44800000, v77
	v_fmamk_f32 v38, v38, 0x44800000, v77
	v_fmamk_f32 v42, v42, 0x44800000, v77
	v_fmamk_f32 v46, v46, 0x44800000, v77
	v_med3_f32 v34, v34, v83, v79
	v_med3_f32 v38, v38, v83, v79
	v_med3_f32 v42, v42, v83, v79
	v_med3_f32 v46, v46, v83, v79
	v_perm_b32 v34, v38, v34, v84
	v_perm_b32 v42, v46, v42, v84
	v_lshl_or_b32 v68, v42, 16, v34
	v_fmamk_f32 v35, v35, 0x44800000, v77
	v_fmamk_f32 v39, v39, 0x44800000, v77
	v_fmamk_f32 v43, v43, 0x44800000, v77
	v_fmamk_f32 v47, v47, 0x44800000, v77
	v_med3_f32 v35, v35, v83, v79
	v_med3_f32 v39, v39, v83, v79
	v_med3_f32 v43, v43, v83, v79
	v_med3_f32 v47, v47, v83, v79
	v_perm_b32 v35, v39, v35, v84
	v_perm_b32 v43, v47, v43, v84
	v_lshl_or_b32 v220, v43, 16, v35
	v_fmamk_f32 v36, v36, 0x44800000, v77
	v_fmamk_f32 v40, v40, 0x44800000, v77
	v_fmamk_f32 v44, v44, 0x44800000, v77
	v_fmamk_f32 v48, v48, 0x44800000, v77
	v_med3_f32 v36, v36, v83, v79
	v_med3_f32 v40, v40, v83, v79
	v_med3_f32 v44, v44, v83, v79
	v_med3_f32 v48, v48, v83, v79
	v_perm_b32 v36, v40, v36, v84
	v_perm_b32 v44, v48, v44, v84
	v_lshl_or_b32 v224, v44, 16, v36
	v_fmamk_f32 v37, v37, 0x44800000, v77
	v_fmamk_f32 v41, v41, 0x44800000, v77
	v_fmamk_f32 v45, v45, 0x44800000, v77
	v_fmamk_f32 v49, v49, 0x44800000, v77
	v_med3_f32 v37, v37, v83, v79
	v_med3_f32 v41, v41, v83, v79
	v_med3_f32 v45, v45, v83, v79
	v_med3_f32 v49, v49, v83, v79
	v_perm_b32 v37, v41, v37, v84
	v_perm_b32 v45, v49, v45, v84
	v_lshl_or_b32 v228, v45, 16, v37
	s_waitcnt vmcnt(0)
	v_fmamk_f32 v50, v50, 0x44800000, v77
	v_fmamk_f32 v54, v54, 0x44800000, v77
	v_fmamk_f32 v58, v58, 0x44800000, v77
	v_fmamk_f32 v62, v62, 0x44800000, v77
	v_med3_f32 v50, v50, v83, v79
	v_med3_f32 v54, v54, v83, v79
	v_med3_f32 v58, v58, v83, v79
	v_med3_f32 v62, v62, v83, v79
	v_perm_b32 v50, v54, v50, v84
	v_perm_b32 v58, v62, v58, v84
	v_lshl_or_b32 v69, v58, 16, v50
	v_fmamk_f32 v51, v51, 0x44800000, v77
	v_fmamk_f32 v55, v55, 0x44800000, v77
	v_fmamk_f32 v59, v59, 0x44800000, v77
	v_fmamk_f32 v63, v63, 0x44800000, v77
	v_med3_f32 v51, v51, v83, v79
	v_med3_f32 v55, v55, v83, v79
	v_med3_f32 v59, v59, v83, v79
	v_med3_f32 v63, v63, v83, v79
	v_perm_b32 v51, v55, v51, v84
	v_perm_b32 v59, v63, v59, v84
	v_lshl_or_b32 v221, v59, 16, v51
	v_fmamk_f32 v52, v52, 0x44800000, v77
	v_fmamk_f32 v56, v56, 0x44800000, v77
	v_fmamk_f32 v60, v60, 0x44800000, v77
	v_fmamk_f32 v64, v64, 0x44800000, v77
	v_med3_f32 v52, v52, v83, v79
	v_med3_f32 v56, v56, v83, v79
	v_med3_f32 v60, v60, v83, v79
	v_med3_f32 v64, v64, v83, v79
	v_perm_b32 v52, v56, v52, v84
	v_perm_b32 v60, v64, v60, v84
	v_lshl_or_b32 v225, v60, 16, v52
	v_fmamk_f32 v53, v53, 0x44800000, v77
	v_fmamk_f32 v57, v57, 0x44800000, v77
	v_fmamk_f32 v61, v61, 0x44800000, v77
	v_fmamk_f32 v65, v65, 0x44800000, v77
	v_med3_f32 v53, v53, v83, v79
	v_med3_f32 v57, v57, v83, v79
	v_med3_f32 v61, v61, v83, v79
	v_med3_f32 v65, v65, v83, v79
	v_perm_b32 v53, v57, v53, v84
	v_perm_b32 v61, v65, v61, v84
	v_lshl_or_b32 v229, v61, 16, v53
	ds_write_b128 v74, v[66:69]
	ds_write_b128 v74, v[218:221] offset:528
	ds_write_b128 v74, v[222:225] offset:1056
	ds_write_b128 v74, v[226:229] offset:1584
	s_mov_b64 s[28:29], 0

.LBB0_2347:
	s_mov_b32 s21, s77
	s_mov_b32 s23, s54
	s_mov_b32 s20, s78
	s_mov_b32 s11, s25
	s_mov_b32 s22, s76
	s_mov_b32 s10, s24
	s_mov_b64 s[26:27], s[52:53]
	s_mov_b64 s[30:31], -1
	s_mov_b64 s[2:3], 0
	s_cmp_lt_i32 s77, 2
	s_mov_b64 s[28:29], 0
	s_cbranch_scc1 .LBB0_2354
	s_cmp_eq_u32 s21, 2
	s_mov_b64 s[28:29], -1
	s_cbranch_scc0 .LBB0_2350
	s_waitcnt vmcnt(12)
	v_mov_b32_e32 v73, 0x4b400000
	v_mov_b32_e32 v74, 0x4b40007f
	v_mov_b32_e32 v75, 0x4b3fff81
	v_mov_b32_e32 v76, 0xc0c0400
	v_add_u32_e32 v70, v199, v198
	v_fmamk_f32 v2, v2, 0x44800000, v73
	v_fmamk_f32 v6, v6, 0x44800000, v73
	v_fmamk_f32 v10, v10, 0x44800000, v73
	v_fmamk_f32 v14, v14, 0x44800000, v73
	v_med3_f32 v2, v2, v75, v74
	v_med3_f32 v6, v6, v75, v74
	v_med3_f32 v10, v10, v75, v74
	v_med3_f32 v14, v14, v75, v74
	v_perm_b32 v2, v6, v2, v76
	v_perm_b32 v10, v14, v10, v76
	v_lshl_or_b32 v66, v10, 16, v2
	v_fmamk_f32 v3, v3, 0x44800000, v73
	v_fmamk_f32 v7, v7, 0x44800000, v73
	v_fmamk_f32 v11, v11, 0x44800000, v73
	v_fmamk_f32 v15, v15, 0x44800000, v73
	v_med3_f32 v3, v3, v75, v74
	v_med3_f32 v7, v7, v75, v74
	v_med3_f32 v11, v11, v75, v74
	v_med3_f32 v15, v15, v75, v74
	v_perm_b32 v3, v7, v3, v76
	v_perm_b32 v11, v15, v11, v76
	v_lshl_or_b32 v218, v11, 16, v3
	v_fmamk_f32 v4, v4, 0x44800000, v73
	v_fmamk_f32 v8, v8, 0x44800000, v73
	v_fmamk_f32 v12, v12, 0x44800000, v73
	v_fmamk_f32 v16, v16, 0x44800000, v73
	v_med3_f32 v4, v4, v75, v74
	v_med3_f32 v8, v8, v75, v74
	v_med3_f32 v12, v12, v75, v74
	v_med3_f32 v16, v16, v75, v74
	v_perm_b32 v4, v8, v4, v76
	v_perm_b32 v12, v16, v12, v76
	v_lshl_or_b32 v222, v12, 16, v4
	v_fmamk_f32 v5, v5, 0x44800000, v73
	v_fmamk_f32 v9, v9, 0x44800000, v73
	v_fmamk_f32 v13, v13, 0x44800000, v73
	v_fmamk_f32 v17, v17, 0x44800000, v73
	v_med3_f32 v5, v5, v75, v74
	v_med3_f32 v9, v9, v75, v74
	v_med3_f32 v13, v13, v75, v74
	v_med3_f32 v17, v17, v75, v74
	v_perm_b32 v5, v9, v5, v76
	v_perm_b32 v13, v17, v13, v76
	v_lshl_or_b32 v226, v13, 16, v5
	s_waitcnt vmcnt(8)
	v_fmamk_f32 v18, v18, 0x44800000, v73
	v_fmamk_f32 v22, v22, 0x44800000, v73
	v_fmamk_f32 v26, v26, 0x44800000, v73
	v_fmamk_f32 v30, v30, 0x44800000, v73
	v_med3_f32 v18, v18, v75, v74
	v_med3_f32 v22, v22, v75, v74
	v_med3_f32 v26, v26, v75, v74
	v_med3_f32 v30, v30, v75, v74
	v_perm_b32 v18, v22, v18, v76
	v_perm_b32 v26, v30, v26, v76
	v_lshl_or_b32 v67, v26, 16, v18
	v_fmamk_f32 v19, v19, 0x44800000, v73
	v_fmamk_f32 v23, v23, 0x44800000, v73
	v_fmamk_f32 v27, v27, 0x44800000, v73
	v_fmamk_f32 v31, v31, 0x44800000, v73
	v_med3_f32 v19, v19, v75, v74
	v_med3_f32 v23, v23, v75, v74
	v_med3_f32 v27, v27, v75, v74
	v_med3_f32 v31, v31, v75, v74
	v_perm_b32 v19, v23, v19, v76
	v_perm_b32 v27, v31, v27, v76
	v_lshl_or_b32 v219, v27, 16, v19
	v_fmamk_f32 v20, v20, 0x44800000, v73
	v_fmamk_f32 v24, v24, 0x44800000, v73
	v_fmamk_f32 v28, v28, 0x44800000, v73
	v_fmamk_f32 v32, v32, 0x44800000, v73
	v_med3_f32 v20, v20, v75, v74
	v_med3_f32 v24, v24, v75, v74
	v_med3_f32 v28, v28, v75, v74
	v_med3_f32 v32, v32, v75, v74
	v_perm_b32 v20, v24, v20, v76
	v_perm_b32 v28, v32, v28, v76
	v_lshl_or_b32 v223, v28, 16, v20
	v_fmamk_f32 v21, v21, 0x44800000, v73
	v_fmamk_f32 v25, v25, 0x44800000, v73
	v_fmamk_f32 v29, v29, 0x44800000, v73
	v_fmamk_f32 v33, v33, 0x44800000, v73
	v_med3_f32 v21, v21, v75, v74
	v_med3_f32 v25, v25, v75, v74
	v_med3_f32 v29, v29, v75, v74
	v_med3_f32 v33, v33, v75, v74
	v_perm_b32 v21, v25, v21, v76
	v_perm_b32 v29, v33, v29, v76
	v_lshl_or_b32 v227, v29, 16, v21
	s_waitcnt vmcnt(4)
	v_fmamk_f32 v34, v34, 0x44800000, v73
	v_fmamk_f32 v38, v38, 0x44800000, v73
	v_fmamk_f32 v42, v42, 0x44800000, v73
	v_fmamk_f32 v46, v46, 0x44800000, v73
	v_med3_f32 v34, v34, v75, v74
	v_med3_f32 v38, v38, v75, v74
	v_med3_f32 v42, v42, v75, v74
	v_med3_f32 v46, v46, v75, v74
	v_perm_b32 v34, v38, v34, v76
	v_perm_b32 v42, v46, v42, v76
	v_lshl_or_b32 v68, v42, 16, v34
	v_fmamk_f32 v35, v35, 0x44800000, v73
	v_fmamk_f32 v39, v39, 0x44800000, v73
	v_fmamk_f32 v43, v43, 0x44800000, v73
	v_fmamk_f32 v47, v47, 0x44800000, v73
	v_med3_f32 v35, v35, v75, v74
	v_med3_f32 v39, v39, v75, v74
	v_med3_f32 v43, v43, v75, v74
	v_med3_f32 v47, v47, v75, v74
	v_perm_b32 v35, v39, v35, v76
	v_perm_b32 v43, v47, v43, v76
	v_lshl_or_b32 v220, v43, 16, v35
	v_fmamk_f32 v36, v36, 0x44800000, v73
	v_fmamk_f32 v40, v40, 0x44800000, v73
	v_fmamk_f32 v44, v44, 0x44800000, v73
	v_fmamk_f32 v48, v48, 0x44800000, v73
	v_med3_f32 v36, v36, v75, v74
	v_med3_f32 v40, v40, v75, v74
	v_med3_f32 v44, v44, v75, v74
	v_med3_f32 v48, v48, v75, v74
	v_perm_b32 v36, v40, v36, v76
	v_perm_b32 v44, v48, v44, v76
	v_lshl_or_b32 v224, v44, 16, v36
	v_fmamk_f32 v37, v37, 0x44800000, v73
	v_fmamk_f32 v41, v41, 0x44800000, v73
	v_fmamk_f32 v45, v45, 0x44800000, v73
	v_fmamk_f32 v49, v49, 0x44800000, v73
	v_med3_f32 v37, v37, v75, v74
	v_med3_f32 v41, v41, v75, v74
	v_med3_f32 v45, v45, v75, v74
	v_med3_f32 v49, v49, v75, v74
	v_perm_b32 v37, v41, v37, v76
	v_perm_b32 v45, v49, v45, v76
	v_lshl_or_b32 v228, v45, 16, v37
	s_waitcnt vmcnt(0)
	v_fmamk_f32 v50, v50, 0x44800000, v73
	v_fmamk_f32 v54, v54, 0x44800000, v73
	v_fmamk_f32 v58, v58, 0x44800000, v73
	v_fmamk_f32 v62, v62, 0x44800000, v73
	v_med3_f32 v50, v50, v75, v74
	v_med3_f32 v54, v54, v75, v74
	v_med3_f32 v58, v58, v75, v74
	v_med3_f32 v62, v62, v75, v74
	v_perm_b32 v50, v54, v50, v76
	v_perm_b32 v58, v62, v58, v76
	v_lshl_or_b32 v69, v58, 16, v50
	v_fmamk_f32 v51, v51, 0x44800000, v73
	v_fmamk_f32 v55, v55, 0x44800000, v73
	v_fmamk_f32 v59, v59, 0x44800000, v73
	v_fmamk_f32 v63, v63, 0x44800000, v73
	v_med3_f32 v51, v51, v75, v74
	v_med3_f32 v55, v55, v75, v74
	v_med3_f32 v59, v59, v75, v74
	v_med3_f32 v63, v63, v75, v74
	v_perm_b32 v51, v55, v51, v76
	v_perm_b32 v59, v63, v59, v76
	v_lshl_or_b32 v221, v59, 16, v51
	v_fmamk_f32 v52, v52, 0x44800000, v73
	v_fmamk_f32 v56, v56, 0x44800000, v73
	v_fmamk_f32 v60, v60, 0x44800000, v73
	v_fmamk_f32 v64, v64, 0x44800000, v73
	v_med3_f32 v52, v52, v75, v74
	v_med3_f32 v56, v56, v75, v74
	v_med3_f32 v60, v60, v75, v74
	v_med3_f32 v64, v64, v75, v74
	v_perm_b32 v52, v56, v52, v76
	v_perm_b32 v60, v64, v60, v76
	v_lshl_or_b32 v225, v60, 16, v52
	v_fmamk_f32 v53, v53, 0x44800000, v73
	v_fmamk_f32 v57, v57, 0x44800000, v73
	v_fmamk_f32 v61, v61, 0x44800000, v73
	v_fmamk_f32 v65, v65, 0x44800000, v73
	v_med3_f32 v53, v53, v75, v74
	v_med3_f32 v57, v57, v75, v74
	v_med3_f32 v61, v61, v75, v74
	v_med3_f32 v65, v65, v75, v74
	v_perm_b32 v53, v57, v53, v76
	v_perm_b32 v61, v65, v61, v76
	v_lshl_or_b32 v229, v61, 16, v53
	ds_write_b128 v70, v[66:69]
	ds_write_b128 v70, v[218:221] offset:528
	ds_write_b128 v70, v[222:225] offset:1056
	ds_write_b128 v70, v[226:229] offset:1584
	s_mov_b64 s[28:29], 0

.LBB0_2641:
	s_mov_b32 s21, s76
	s_mov_b32 s23, s54
	s_mov_b32 s20, s77
	s_mov_b32 s11, s25
	s_mov_b32 s22, s71
	s_mov_b32 s10, s24
	s_mov_b64 s[26:27], s[52:53]
	s_mov_b64 s[30:31], -1
	s_mov_b64 s[2:3], 0
	s_cmp_lt_i32 s76, 2
	s_mov_b64 s[28:29], 0
	s_cbranch_scc1 .LBB0_2648
	s_cmp_eq_u32 s21, 2
	s_mov_b64 s[28:29], -1
	s_cbranch_scc0 .LBB0_2644
	s_waitcnt vmcnt(12)
	v_mov_b32_e32 v73, 0x4b400000
	v_mov_b32_e32 v74, 0x4b40007f
	v_mov_b32_e32 v75, 0x4b3fff81
	v_mov_b32_e32 v76, 0xc0c0400
	v_add_u32_e32 v70, v199, v198
	v_fmamk_f32 v2, v2, 0x44800000, v73
	v_fmamk_f32 v6, v6, 0x44800000, v73
	v_fmamk_f32 v10, v10, 0x44800000, v73
	v_fmamk_f32 v14, v14, 0x44800000, v73
	v_med3_f32 v2, v2, v75, v74
	v_med3_f32 v6, v6, v75, v74
	v_med3_f32 v10, v10, v75, v74
	v_med3_f32 v14, v14, v75, v74
	v_perm_b32 v2, v6, v2, v76
	v_perm_b32 v10, v14, v10, v76
	v_lshl_or_b32 v66, v10, 16, v2
	v_fmamk_f32 v3, v3, 0x44800000, v73
	v_fmamk_f32 v7, v7, 0x44800000, v73
	v_fmamk_f32 v11, v11, 0x44800000, v73
	v_fmamk_f32 v15, v15, 0x44800000, v73
	v_med3_f32 v3, v3, v75, v74
	v_med3_f32 v7, v7, v75, v74
	v_med3_f32 v11, v11, v75, v74
	v_med3_f32 v15, v15, v75, v74
	v_perm_b32 v3, v7, v3, v76
	v_perm_b32 v11, v15, v11, v76
	v_lshl_or_b32 v218, v11, 16, v3
	v_fmamk_f32 v4, v4, 0x44800000, v73
	v_fmamk_f32 v8, v8, 0x44800000, v73
	v_fmamk_f32 v12, v12, 0x44800000, v73
	v_fmamk_f32 v16, v16, 0x44800000, v73
	v_med3_f32 v4, v4, v75, v74
	v_med3_f32 v8, v8, v75, v74
	v_med3_f32 v12, v12, v75, v74
	v_med3_f32 v16, v16, v75, v74
	v_perm_b32 v4, v8, v4, v76
	v_perm_b32 v12, v16, v12, v76
	v_lshl_or_b32 v222, v12, 16, v4
	v_fmamk_f32 v5, v5, 0x44800000, v73
	v_fmamk_f32 v9, v9, 0x44800000, v73
	v_fmamk_f32 v13, v13, 0x44800000, v73
	v_fmamk_f32 v17, v17, 0x44800000, v73
	v_med3_f32 v5, v5, v75, v74
	v_med3_f32 v9, v9, v75, v74
	v_med3_f32 v13, v13, v75, v74
	v_med3_f32 v17, v17, v75, v74
	v_perm_b32 v5, v9, v5, v76
	v_perm_b32 v13, v17, v13, v76
	v_lshl_or_b32 v226, v13, 16, v5
	s_waitcnt vmcnt(8)
	v_fmamk_f32 v18, v18, 0x44800000, v73
	v_fmamk_f32 v22, v22, 0x44800000, v73
	v_fmamk_f32 v26, v26, 0x44800000, v73
	v_fmamk_f32 v30, v30, 0x44800000, v73
	v_med3_f32 v18, v18, v75, v74
	v_med3_f32 v22, v22, v75, v74
	v_med3_f32 v26, v26, v75, v74
	v_med3_f32 v30, v30, v75, v74
	v_perm_b32 v18, v22, v18, v76
	v_perm_b32 v26, v30, v26, v76
	v_lshl_or_b32 v67, v26, 16, v18
	v_fmamk_f32 v19, v19, 0x44800000, v73
	v_fmamk_f32 v23, v23, 0x44800000, v73
	v_fmamk_f32 v27, v27, 0x44800000, v73
	v_fmamk_f32 v31, v31, 0x44800000, v73
	v_med3_f32 v19, v19, v75, v74
	v_med3_f32 v23, v23, v75, v74
	v_med3_f32 v27, v27, v75, v74
	v_med3_f32 v31, v31, v75, v74
	v_perm_b32 v19, v23, v19, v76
	v_perm_b32 v27, v31, v27, v76
	v_lshl_or_b32 v219, v27, 16, v19
	v_fmamk_f32 v20, v20, 0x44800000, v73
	v_fmamk_f32 v24, v24, 0x44800000, v73
	v_fmamk_f32 v28, v28, 0x44800000, v73
	v_fmamk_f32 v32, v32, 0x44800000, v73
	v_med3_f32 v20, v20, v75, v74
	v_med3_f32 v24, v24, v75, v74
	v_med3_f32 v28, v28, v75, v74
	v_med3_f32 v32, v32, v75, v74
	v_perm_b32 v20, v24, v20, v76
	v_perm_b32 v28, v32, v28, v76
	v_lshl_or_b32 v223, v28, 16, v20
	v_fmamk_f32 v21, v21, 0x44800000, v73
	v_fmamk_f32 v25, v25, 0x44800000, v73
	v_fmamk_f32 v29, v29, 0x44800000, v73
	v_fmamk_f32 v33, v33, 0x44800000, v73
	v_med3_f32 v21, v21, v75, v74
	v_med3_f32 v25, v25, v75, v74
	v_med3_f32 v29, v29, v75, v74
	v_med3_f32 v33, v33, v75, v74
	v_perm_b32 v21, v25, v21, v76
	v_perm_b32 v29, v33, v29, v76
	v_lshl_or_b32 v227, v29, 16, v21
	s_waitcnt vmcnt(4)
	v_fmamk_f32 v34, v34, 0x44800000, v73
	v_fmamk_f32 v38, v38, 0x44800000, v73
	v_fmamk_f32 v42, v42, 0x44800000, v73
	v_fmamk_f32 v46, v46, 0x44800000, v73
	v_med3_f32 v34, v34, v75, v74
	v_med3_f32 v38, v38, v75, v74
	v_med3_f32 v42, v42, v75, v74
	v_med3_f32 v46, v46, v75, v74
	v_perm_b32 v34, v38, v34, v76
	v_perm_b32 v42, v46, v42, v76
	v_lshl_or_b32 v68, v42, 16, v34
	v_fmamk_f32 v35, v35, 0x44800000, v73
	v_fmamk_f32 v39, v39, 0x44800000, v73
	v_fmamk_f32 v43, v43, 0x44800000, v73
	v_fmamk_f32 v47, v47, 0x44800000, v73
	v_med3_f32 v35, v35, v75, v74
	v_med3_f32 v39, v39, v75, v74
	v_med3_f32 v43, v43, v75, v74
	v_med3_f32 v47, v47, v75, v74
	v_perm_b32 v35, v39, v35, v76
	v_perm_b32 v43, v47, v43, v76
	v_lshl_or_b32 v220, v43, 16, v35
	v_fmamk_f32 v36, v36, 0x44800000, v73
	v_fmamk_f32 v40, v40, 0x44800000, v73
	v_fmamk_f32 v44, v44, 0x44800000, v73
	v_fmamk_f32 v48, v48, 0x44800000, v73
	v_med3_f32 v36, v36, v75, v74
	v_med3_f32 v40, v40, v75, v74
	v_med3_f32 v44, v44, v75, v74
	v_med3_f32 v48, v48, v75, v74
	v_perm_b32 v36, v40, v36, v76
	v_perm_b32 v44, v48, v44, v76
	v_lshl_or_b32 v224, v44, 16, v36
	v_fmamk_f32 v37, v37, 0x44800000, v73
	v_fmamk_f32 v41, v41, 0x44800000, v73
	v_fmamk_f32 v45, v45, 0x44800000, v73
	v_fmamk_f32 v49, v49, 0x44800000, v73
	v_med3_f32 v37, v37, v75, v74
	v_med3_f32 v41, v41, v75, v74
	v_med3_f32 v45, v45, v75, v74
	v_med3_f32 v49, v49, v75, v74
	v_perm_b32 v37, v41, v37, v76
	v_perm_b32 v45, v49, v45, v76
	v_lshl_or_b32 v228, v45, 16, v37
	s_waitcnt vmcnt(0)
	v_fmamk_f32 v50, v50, 0x44800000, v73
	v_fmamk_f32 v54, v54, 0x44800000, v73
	v_fmamk_f32 v58, v58, 0x44800000, v73
	v_fmamk_f32 v62, v62, 0x44800000, v73
	v_med3_f32 v50, v50, v75, v74
	v_med3_f32 v54, v54, v75, v74
	v_med3_f32 v58, v58, v75, v74
	v_med3_f32 v62, v62, v75, v74
	v_perm_b32 v50, v54, v50, v76
	v_perm_b32 v58, v62, v58, v76
	v_lshl_or_b32 v69, v58, 16, v50
	v_fmamk_f32 v51, v51, 0x44800000, v73
	v_fmamk_f32 v55, v55, 0x44800000, v73
	v_fmamk_f32 v59, v59, 0x44800000, v73
	v_fmamk_f32 v63, v63, 0x44800000, v73
	v_med3_f32 v51, v51, v75, v74
	v_med3_f32 v55, v55, v75, v74
	v_med3_f32 v59, v59, v75, v74
	v_med3_f32 v63, v63, v75, v74
	v_perm_b32 v51, v55, v51, v76
	v_perm_b32 v59, v63, v59, v76
	v_lshl_or_b32 v221, v59, 16, v51
	v_fmamk_f32 v52, v52, 0x44800000, v73
	v_fmamk_f32 v56, v56, 0x44800000, v73
	v_fmamk_f32 v60, v60, 0x44800000, v73
	v_fmamk_f32 v64, v64, 0x44800000, v73
	v_med3_f32 v52, v52, v75, v74
	v_med3_f32 v56, v56, v75, v74
	v_med3_f32 v60, v60, v75, v74
	v_med3_f32 v64, v64, v75, v74
	v_perm_b32 v52, v56, v52, v76
	v_perm_b32 v60, v64, v60, v76
	v_lshl_or_b32 v225, v60, 16, v52
	v_fmamk_f32 v53, v53, 0x44800000, v73
	v_fmamk_f32 v57, v57, 0x44800000, v73
	v_fmamk_f32 v61, v61, 0x44800000, v73
	v_fmamk_f32 v65, v65, 0x44800000, v73
	v_med3_f32 v53, v53, v75, v74
	v_med3_f32 v57, v57, v75, v74
	v_med3_f32 v61, v61, v75, v74
	v_med3_f32 v65, v65, v75, v74
	v_perm_b32 v53, v57, v53, v76
	v_perm_b32 v61, v65, v61, v76
	v_lshl_or_b32 v229, v61, 16, v53
	ds_write_b128 v70, v[66:69]
	ds_write_b128 v70, v[218:221] offset:528
	ds_write_b128 v70, v[222:225] offset:1056
	ds_write_b128 v70, v[226:229] offset:1584
	s_mov_b64 s[28:29], 0

.LBB0_3185:
	s_mov_b32 s17, s68
	s_mov_b32 s64, s22
	s_mov_b32 s16, s69
	s_mov_b32 s25, s66
	s_mov_b32 s63, s67
	s_mov_b32 s24, s65
	s_mov_b64 s[18:19], s[20:21]
	s_mov_b64 s[22:23], -1
	s_mov_b64 s[2:3], 0
	s_cmp_lt_i32 s68, 2
	s_mov_b64 s[20:21], 0
	s_cbranch_scc1 .LBB0_3192
	s_cmp_eq_u32 s17, 2
	s_mov_b64 s[20:21], -1
	s_cbranch_scc0 .LBB0_3188
	s_waitcnt vmcnt(12)
	v_mov_b32_e32 v76, 0x4b400000
	v_mov_b32_e32 v77, 0x4b40007f
	v_mov_b32_e32 v90, 0x4b3fff81
	v_mov_b32_e32 v91, 0xc0c0400
	v_add_u32_e32 v89, v78, v75
	v_fmamk_f32 v2, v2, 0x44800000, v76
	v_fmamk_f32 v6, v6, 0x44800000, v76
	v_fmamk_f32 v10, v10, 0x44800000, v76
	v_fmamk_f32 v14, v14, 0x44800000, v76
	v_med3_f32 v2, v2, v90, v77
	v_med3_f32 v6, v6, v90, v77
	v_med3_f32 v10, v10, v90, v77
	v_med3_f32 v14, v14, v90, v77
	v_perm_b32 v2, v6, v2, v91
	v_perm_b32 v10, v14, v10, v91
	v_lshl_or_b32 v66, v10, 16, v2
	v_fmamk_f32 v3, v3, 0x44800000, v76
	v_fmamk_f32 v7, v7, 0x44800000, v76
	v_fmamk_f32 v11, v11, 0x44800000, v76
	v_fmamk_f32 v15, v15, 0x44800000, v76
	v_med3_f32 v3, v3, v90, v77
	v_med3_f32 v7, v7, v90, v77
	v_med3_f32 v11, v11, v90, v77
	v_med3_f32 v15, v15, v90, v77
	v_perm_b32 v3, v7, v3, v91
	v_perm_b32 v11, v15, v11, v91
	v_lshl_or_b32 v218, v11, 16, v3
	v_fmamk_f32 v4, v4, 0x44800000, v76
	v_fmamk_f32 v8, v8, 0x44800000, v76
	v_fmamk_f32 v12, v12, 0x44800000, v76
	v_fmamk_f32 v16, v16, 0x44800000, v76
	v_med3_f32 v4, v4, v90, v77
	v_med3_f32 v8, v8, v90, v77
	v_med3_f32 v12, v12, v90, v77
	v_med3_f32 v16, v16, v90, v77
	v_perm_b32 v4, v8, v4, v91
	v_perm_b32 v12, v16, v12, v91
	v_lshl_or_b32 v222, v12, 16, v4
	v_fmamk_f32 v5, v5, 0x44800000, v76
	v_fmamk_f32 v9, v9, 0x44800000, v76
	v_fmamk_f32 v13, v13, 0x44800000, v76
	v_fmamk_f32 v17, v17, 0x44800000, v76
	v_med3_f32 v5, v5, v90, v77
	v_med3_f32 v9, v9, v90, v77
	v_med3_f32 v13, v13, v90, v77
	v_med3_f32 v17, v17, v90, v77
	v_perm_b32 v5, v9, v5, v91
	v_perm_b32 v13, v17, v13, v91
	v_lshl_or_b32 v226, v13, 16, v5
	s_waitcnt vmcnt(8)
	v_fmamk_f32 v18, v18, 0x44800000, v76
	v_fmamk_f32 v22, v22, 0x44800000, v76
	v_fmamk_f32 v26, v26, 0x44800000, v76
	v_fmamk_f32 v30, v30, 0x44800000, v76
	v_med3_f32 v18, v18, v90, v77
	v_med3_f32 v22, v22, v90, v77
	v_med3_f32 v26, v26, v90, v77
	v_med3_f32 v30, v30, v90, v77
	v_perm_b32 v18, v22, v18, v91
	v_perm_b32 v26, v30, v26, v91
	v_lshl_or_b32 v67, v26, 16, v18
	v_fmamk_f32 v19, v19, 0x44800000, v76
	v_fmamk_f32 v23, v23, 0x44800000, v76
	v_fmamk_f32 v27, v27, 0x44800000, v76
	v_fmamk_f32 v31, v31, 0x44800000, v76
	v_med3_f32 v19, v19, v90, v77
	v_med3_f32 v23, v23, v90, v77
	v_med3_f32 v27, v27, v90, v77
	v_med3_f32 v31, v31, v90, v77
	v_perm_b32 v19, v23, v19, v91
	v_perm_b32 v27, v31, v27, v91
	v_lshl_or_b32 v219, v27, 16, v19
	v_fmamk_f32 v20, v20, 0x44800000, v76
	v_fmamk_f32 v24, v24, 0x44800000, v76
	v_fmamk_f32 v28, v28, 0x44800000, v76
	v_fmamk_f32 v32, v32, 0x44800000, v76
	v_med3_f32 v20, v20, v90, v77
	v_med3_f32 v24, v24, v90, v77
	v_med3_f32 v28, v28, v90, v77
	v_med3_f32 v32, v32, v90, v77
	v_perm_b32 v20, v24, v20, v91
	v_perm_b32 v28, v32, v28, v91
	v_lshl_or_b32 v223, v28, 16, v20
	v_fmamk_f32 v21, v21, 0x44800000, v76
	v_fmamk_f32 v25, v25, 0x44800000, v76
	v_fmamk_f32 v29, v29, 0x44800000, v76
	v_fmamk_f32 v33, v33, 0x44800000, v76
	v_med3_f32 v21, v21, v90, v77
	v_med3_f32 v25, v25, v90, v77
	v_med3_f32 v29, v29, v90, v77
	v_med3_f32 v33, v33, v90, v77
	v_perm_b32 v21, v25, v21, v91
	v_perm_b32 v29, v33, v29, v91
	v_lshl_or_b32 v227, v29, 16, v21
	s_waitcnt vmcnt(4)
	v_fmamk_f32 v34, v34, 0x44800000, v76
	v_fmamk_f32 v38, v38, 0x44800000, v76
	v_fmamk_f32 v42, v42, 0x44800000, v76
	v_fmamk_f32 v46, v46, 0x44800000, v76
	v_med3_f32 v34, v34, v90, v77
	v_med3_f32 v38, v38, v90, v77
	v_med3_f32 v42, v42, v90, v77
	v_med3_f32 v46, v46, v90, v77
	v_perm_b32 v34, v38, v34, v91
	v_perm_b32 v42, v46, v42, v91
	v_lshl_or_b32 v68, v42, 16, v34
	v_fmamk_f32 v35, v35, 0x44800000, v76
	v_fmamk_f32 v39, v39, 0x44800000, v76
	v_fmamk_f32 v43, v43, 0x44800000, v76
	v_fmamk_f32 v47, v47, 0x44800000, v76
	v_med3_f32 v35, v35, v90, v77
	v_med3_f32 v39, v39, v90, v77
	v_med3_f32 v43, v43, v90, v77
	v_med3_f32 v47, v47, v90, v77
	v_perm_b32 v35, v39, v35, v91
	v_perm_b32 v43, v47, v43, v91
	v_lshl_or_b32 v220, v43, 16, v35
	v_fmamk_f32 v36, v36, 0x44800000, v76
	v_fmamk_f32 v40, v40, 0x44800000, v76
	v_fmamk_f32 v44, v44, 0x44800000, v76
	v_fmamk_f32 v48, v48, 0x44800000, v76
	v_med3_f32 v36, v36, v90, v77
	v_med3_f32 v40, v40, v90, v77
	v_med3_f32 v44, v44, v90, v77
	v_med3_f32 v48, v48, v90, v77
	v_perm_b32 v36, v40, v36, v91
	v_perm_b32 v44, v48, v44, v91
	v_lshl_or_b32 v224, v44, 16, v36
	v_fmamk_f32 v37, v37, 0x44800000, v76
	v_fmamk_f32 v41, v41, 0x44800000, v76
	v_fmamk_f32 v45, v45, 0x44800000, v76
	v_fmamk_f32 v49, v49, 0x44800000, v76
	v_med3_f32 v37, v37, v90, v77
	v_med3_f32 v41, v41, v90, v77
	v_med3_f32 v45, v45, v90, v77
	v_med3_f32 v49, v49, v90, v77
	v_perm_b32 v37, v41, v37, v91
	v_perm_b32 v45, v49, v45, v91
	v_lshl_or_b32 v228, v45, 16, v37
	s_waitcnt vmcnt(0)
	v_fmamk_f32 v50, v50, 0x44800000, v76
	v_fmamk_f32 v54, v54, 0x44800000, v76
	v_fmamk_f32 v58, v58, 0x44800000, v76
	v_fmamk_f32 v62, v62, 0x44800000, v76
	v_med3_f32 v50, v50, v90, v77
	v_med3_f32 v54, v54, v90, v77
	v_med3_f32 v58, v58, v90, v77
	v_med3_f32 v62, v62, v90, v77
	v_perm_b32 v50, v54, v50, v91
	v_perm_b32 v58, v62, v58, v91
	v_lshl_or_b32 v69, v58, 16, v50
	v_fmamk_f32 v51, v51, 0x44800000, v76
	v_fmamk_f32 v55, v55, 0x44800000, v76
	v_fmamk_f32 v59, v59, 0x44800000, v76
	v_fmamk_f32 v63, v63, 0x44800000, v76
	v_med3_f32 v51, v51, v90, v77
	v_med3_f32 v55, v55, v90, v77
	v_med3_f32 v59, v59, v90, v77
	v_med3_f32 v63, v63, v90, v77
	v_perm_b32 v51, v55, v51, v91
	v_perm_b32 v59, v63, v59, v91
	v_lshl_or_b32 v221, v59, 16, v51
	v_fmamk_f32 v52, v52, 0x44800000, v76
	v_fmamk_f32 v56, v56, 0x44800000, v76
	v_fmamk_f32 v60, v60, 0x44800000, v76
	v_fmamk_f32 v64, v64, 0x44800000, v76
	v_med3_f32 v52, v52, v90, v77
	v_med3_f32 v56, v56, v90, v77
	v_med3_f32 v60, v60, v90, v77
	v_med3_f32 v64, v64, v90, v77
	v_perm_b32 v52, v56, v52, v91
	v_perm_b32 v60, v64, v60, v91
	v_lshl_or_b32 v225, v60, 16, v52
	v_fmamk_f32 v53, v53, 0x44800000, v76
	v_fmamk_f32 v57, v57, 0x44800000, v76
	v_fmamk_f32 v61, v61, 0x44800000, v76
	v_fmamk_f32 v65, v65, 0x44800000, v76
	v_med3_f32 v53, v53, v90, v77
	v_med3_f32 v57, v57, v90, v77
	v_med3_f32 v61, v61, v90, v77
	v_med3_f32 v65, v65, v90, v77
	v_perm_b32 v53, v57, v53, v91
	v_perm_b32 v61, v65, v61, v91
	v_lshl_or_b32 v229, v61, 16, v53
	ds_write_b128 v89, v[66:69]
	ds_write_b128 v89, v[218:221] offset:528
	ds_write_b128 v89, v[222:225] offset:1056
	ds_write_b128 v89, v[226:229] offset:1584
	s_mov_b64 s[20:21], 0

.LBB0_3427:
	s_mov_b32 s15, s65
	s_mov_b32 s61, s20
	s_mov_b32 s14, s66
	s_mov_b32 s25, s63
	s_mov_b32 s60, s64
	s_mov_b32 s24, s62
	s_mov_b64 s[16:17], s[18:19]
	s_mov_b64 s[20:21], -1
	s_mov_b64 s[2:3], 0
	s_cmp_lt_i32 s65, 2
	s_mov_b64 s[18:19], 0
	s_cbranch_scc1 .LBB0_3434
	s_cmp_eq_u32 s15, 2
	s_mov_b64 s[18:19], -1
	s_cbranch_scc0 .LBB0_3430
	s_waitcnt vmcnt(12)
	v_mov_b32_e32 v76, 0x4b400000
	v_mov_b32_e32 v77, 0x4b40007f
	v_mov_b32_e32 v90, 0x4b3fff81
	v_mov_b32_e32 v91, 0xc0c0400
	v_add_u32_e32 v89, v78, v75
	v_fmamk_f32 v2, v2, 0x44800000, v76
	v_fmamk_f32 v6, v6, 0x44800000, v76
	v_fmamk_f32 v10, v10, 0x44800000, v76
	v_fmamk_f32 v14, v14, 0x44800000, v76
	v_med3_f32 v2, v2, v90, v77
	v_med3_f32 v6, v6, v90, v77
	v_med3_f32 v10, v10, v90, v77
	v_med3_f32 v14, v14, v90, v77
	v_perm_b32 v2, v6, v2, v91
	v_perm_b32 v10, v14, v10, v91
	v_lshl_or_b32 v66, v10, 16, v2
	v_fmamk_f32 v3, v3, 0x44800000, v76
	v_fmamk_f32 v7, v7, 0x44800000, v76
	v_fmamk_f32 v11, v11, 0x44800000, v76
	v_fmamk_f32 v15, v15, 0x44800000, v76
	v_med3_f32 v3, v3, v90, v77
	v_med3_f32 v7, v7, v90, v77
	v_med3_f32 v11, v11, v90, v77
	v_med3_f32 v15, v15, v90, v77
	v_perm_b32 v3, v7, v3, v91
	v_perm_b32 v11, v15, v11, v91
	v_lshl_or_b32 v218, v11, 16, v3
	v_fmamk_f32 v4, v4, 0x44800000, v76
	v_fmamk_f32 v8, v8, 0x44800000, v76
	v_fmamk_f32 v12, v12, 0x44800000, v76
	v_fmamk_f32 v16, v16, 0x44800000, v76
	v_med3_f32 v4, v4, v90, v77
	v_med3_f32 v8, v8, v90, v77
	v_med3_f32 v12, v12, v90, v77
	v_med3_f32 v16, v16, v90, v77
	v_perm_b32 v4, v8, v4, v91
	v_perm_b32 v12, v16, v12, v91
	v_lshl_or_b32 v222, v12, 16, v4
	v_fmamk_f32 v5, v5, 0x44800000, v76
	v_fmamk_f32 v9, v9, 0x44800000, v76
	v_fmamk_f32 v13, v13, 0x44800000, v76
	v_fmamk_f32 v17, v17, 0x44800000, v76
	v_med3_f32 v5, v5, v90, v77
	v_med3_f32 v9, v9, v90, v77
	v_med3_f32 v13, v13, v90, v77
	v_med3_f32 v17, v17, v90, v77
	v_perm_b32 v5, v9, v5, v91
	v_perm_b32 v13, v17, v13, v91
	v_lshl_or_b32 v226, v13, 16, v5
	s_waitcnt vmcnt(8)
	v_fmamk_f32 v18, v18, 0x44800000, v76
	v_fmamk_f32 v22, v22, 0x44800000, v76
	v_fmamk_f32 v26, v26, 0x44800000, v76
	v_fmamk_f32 v30, v30, 0x44800000, v76
	v_med3_f32 v18, v18, v90, v77
	v_med3_f32 v22, v22, v90, v77
	v_med3_f32 v26, v26, v90, v77
	v_med3_f32 v30, v30, v90, v77
	v_perm_b32 v18, v22, v18, v91
	v_perm_b32 v26, v30, v26, v91
	v_lshl_or_b32 v67, v26, 16, v18
	v_fmamk_f32 v19, v19, 0x44800000, v76
	v_fmamk_f32 v23, v23, 0x44800000, v76
	v_fmamk_f32 v27, v27, 0x44800000, v76
	v_fmamk_f32 v31, v31, 0x44800000, v76
	v_med3_f32 v19, v19, v90, v77
	v_med3_f32 v23, v23, v90, v77
	v_med3_f32 v27, v27, v90, v77
	v_med3_f32 v31, v31, v90, v77
	v_perm_b32 v19, v23, v19, v91
	v_perm_b32 v27, v31, v27, v91
	v_lshl_or_b32 v219, v27, 16, v19
	v_fmamk_f32 v20, v20, 0x44800000, v76
	v_fmamk_f32 v24, v24, 0x44800000, v76
	v_fmamk_f32 v28, v28, 0x44800000, v76
	v_fmamk_f32 v32, v32, 0x44800000, v76
	v_med3_f32 v20, v20, v90, v77
	v_med3_f32 v24, v24, v90, v77
	v_med3_f32 v28, v28, v90, v77
	v_med3_f32 v32, v32, v90, v77
	v_perm_b32 v20, v24, v20, v91
	v_perm_b32 v28, v32, v28, v91
	v_lshl_or_b32 v223, v28, 16, v20
	v_fmamk_f32 v21, v21, 0x44800000, v76
	v_fmamk_f32 v25, v25, 0x44800000, v76
	v_fmamk_f32 v29, v29, 0x44800000, v76
	v_fmamk_f32 v33, v33, 0x44800000, v76
	v_med3_f32 v21, v21, v90, v77
	v_med3_f32 v25, v25, v90, v77
	v_med3_f32 v29, v29, v90, v77
	v_med3_f32 v33, v33, v90, v77
	v_perm_b32 v21, v25, v21, v91
	v_perm_b32 v29, v33, v29, v91
	v_lshl_or_b32 v227, v29, 16, v21
	s_waitcnt vmcnt(4)
	v_fmamk_f32 v34, v34, 0x44800000, v76
	v_fmamk_f32 v38, v38, 0x44800000, v76
	v_fmamk_f32 v42, v42, 0x44800000, v76
	v_fmamk_f32 v46, v46, 0x44800000, v76
	v_med3_f32 v34, v34, v90, v77
	v_med3_f32 v38, v38, v90, v77
	v_med3_f32 v42, v42, v90, v77
	v_med3_f32 v46, v46, v90, v77
	v_perm_b32 v34, v38, v34, v91
	v_perm_b32 v42, v46, v42, v91
	v_lshl_or_b32 v68, v42, 16, v34
	v_fmamk_f32 v35, v35, 0x44800000, v76
	v_fmamk_f32 v39, v39, 0x44800000, v76
	v_fmamk_f32 v43, v43, 0x44800000, v76
	v_fmamk_f32 v47, v47, 0x44800000, v76
	v_med3_f32 v35, v35, v90, v77
	v_med3_f32 v39, v39, v90, v77
	v_med3_f32 v43, v43, v90, v77
	v_med3_f32 v47, v47, v90, v77
	v_perm_b32 v35, v39, v35, v91
	v_perm_b32 v43, v47, v43, v91
	v_lshl_or_b32 v220, v43, 16, v35
	v_fmamk_f32 v36, v36, 0x44800000, v76
	v_fmamk_f32 v40, v40, 0x44800000, v76
	v_fmamk_f32 v44, v44, 0x44800000, v76
	v_fmamk_f32 v48, v48, 0x44800000, v76
	v_med3_f32 v36, v36, v90, v77
	v_med3_f32 v40, v40, v90, v77
	v_med3_f32 v44, v44, v90, v77
	v_med3_f32 v48, v48, v90, v77
	v_perm_b32 v36, v40, v36, v91
	v_perm_b32 v44, v48, v44, v91
	v_lshl_or_b32 v224, v44, 16, v36
	v_fmamk_f32 v37, v37, 0x44800000, v76
	v_fmamk_f32 v41, v41, 0x44800000, v76
	v_fmamk_f32 v45, v45, 0x44800000, v76
	v_fmamk_f32 v49, v49, 0x44800000, v76
	v_med3_f32 v37, v37, v90, v77
	v_med3_f32 v41, v41, v90, v77
	v_med3_f32 v45, v45, v90, v77
	v_med3_f32 v49, v49, v90, v77
	v_perm_b32 v37, v41, v37, v91
	v_perm_b32 v45, v49, v45, v91
	v_lshl_or_b32 v228, v45, 16, v37
	s_waitcnt vmcnt(0)
	v_fmamk_f32 v50, v50, 0x44800000, v76
	v_fmamk_f32 v54, v54, 0x44800000, v76
	v_fmamk_f32 v58, v58, 0x44800000, v76
	v_fmamk_f32 v62, v62, 0x44800000, v76
	v_med3_f32 v50, v50, v90, v77
	v_med3_f32 v54, v54, v90, v77
	v_med3_f32 v58, v58, v90, v77
	v_med3_f32 v62, v62, v90, v77
	v_perm_b32 v50, v54, v50, v91
	v_perm_b32 v58, v62, v58, v91
	v_lshl_or_b32 v69, v58, 16, v50
	v_fmamk_f32 v51, v51, 0x44800000, v76
	v_fmamk_f32 v55, v55, 0x44800000, v76
	v_fmamk_f32 v59, v59, 0x44800000, v76
	v_fmamk_f32 v63, v63, 0x44800000, v76
	v_med3_f32 v51, v51, v90, v77
	v_med3_f32 v55, v55, v90, v77
	v_med3_f32 v59, v59, v90, v77
	v_med3_f32 v63, v63, v90, v77
	v_perm_b32 v51, v55, v51, v91
	v_perm_b32 v59, v63, v59, v91
	v_lshl_or_b32 v221, v59, 16, v51
	v_fmamk_f32 v52, v52, 0x44800000, v76
	v_fmamk_f32 v56, v56, 0x44800000, v76
	v_fmamk_f32 v60, v60, 0x44800000, v76
	v_fmamk_f32 v64, v64, 0x44800000, v76
	v_med3_f32 v52, v52, v90, v77
	v_med3_f32 v56, v56, v90, v77
	v_med3_f32 v60, v60, v90, v77
	v_med3_f32 v64, v64, v90, v77
	v_perm_b32 v52, v56, v52, v91
	v_perm_b32 v60, v64, v60, v91
	v_lshl_or_b32 v225, v60, 16, v52
	v_fmamk_f32 v53, v53, 0x44800000, v76
	v_fmamk_f32 v57, v57, 0x44800000, v76
	v_fmamk_f32 v61, v61, 0x44800000, v76
	v_fmamk_f32 v65, v65, 0x44800000, v76
	v_med3_f32 v53, v53, v90, v77
	v_med3_f32 v57, v57, v90, v77
	v_med3_f32 v61, v61, v90, v77
	v_med3_f32 v65, v65, v90, v77
	v_perm_b32 v53, v57, v53, v91
	v_perm_b32 v61, v65, v61, v91
	v_lshl_or_b32 v229, v61, 16, v53
	ds_write_b128 v89, v[66:69]
	ds_write_b128 v89, v[218:221] offset:528
	ds_write_b128 v89, v[222:225] offset:1056
	ds_write_b128 v89, v[226:229] offset:1584
	s_mov_b64 s[18:19], 0
